# v1 + nt (non-temporal) cache policy on the expert weight conversion f32 loads (read-once stream)
# baseline (speedup 1.0000x reference)
.LBB0_219:
	s_add_u32 s7, s82, 0x4000000
	v_readlane_b32 s34, v252, 14
	s_waitcnt lgkmcnt(0)
	s_addc_u32 s10, s83, 0
	s_ashr_i32 s0, s34, 31
	s_lshr_b32 s0, s0, 23
	s_add_i32 s2, s34, s0
	s_ashr_i32 s0, s2, 9
	s_ashr_i32 s1, s0, 31
	s_lshl_b64 s[0:1], s[0:1], 25
	s_add_u32 s0, s16, s0
	s_addc_u32 s1, s17, s1
	s_and_b32 s2, s2, 0xfffffe00
	s_sub_i32 s2, s34, s2
	s_lshr_b32 s3, s2, 3
	s_bfe_i32 s4, s3, 0x80000
	s_bfe_u32 s4, s4, 0x2000d
	s_add_i32 s4, s3, s4
	s_bfe_i32 s5, s4, 0x80000
	s_and_b32 s4, s4, 0xfc
	s_sub_i32 s3, s3, s4
	s_sext_i32_i8 s3, s3
	s_lshl_b32 s2, s2, 6
	s_lshl_b32 s3, s3, 9
	s_and_b32 s4, s2, 0x100
	s_sext_i32_i16 s5, s5
	s_or_b32 s3, s3, s4
	v_and_b32_e32 v137, 48, v0
	s_waitcnt vmcnt(39)
	v_or_b32_e32 v42, s3, v137
	s_lshl_b32 s3, s5, 6
	s_and_b32 s3, s3, 0xffffff00
	s_and_b32 s2, s2, 0xc0
	v_ashrrev_i32_e32 v43, 31, v42
	s_or_b32 s2, s3, s2
	v_lshlrev_b64 v[2:3], 14, v[42:43]
	s_ashr_i32 s3, s2, 31
	v_and_b32_e32 v1, 15, v0
	v_lshl_add_u64 v[2:3], s[0:1], 0, v[2:3]
	s_lshl_b64 s[2:3], s[2:3], 2
	v_mov_b32_e32 v131, 0
	v_lshl_add_u64 v[2:3], v[2:3], 0, s[2:3]
	v_lshlrev_b32_e32 v132, 4, v1
	v_mov_b32_e32 v133, v131
	s_waitcnt vmcnt(35)
	v_lshl_add_u64 v[44:45], v[2:3], 0, v[132:133]
	s_movk_i32 s11, 0x4000
	v_add_co_u32_e32 v10, vcc, s11, v44
	s_mov_b32 s18, 0x8000
	s_nop 0
	v_addc_co_u32_e32 v11, vcc, 0, v45, vcc
	v_add_co_u32_e32 v14, vcc, s18, v44
	s_mov_b32 s19, 0xc000
	s_nop 0
	v_addc_co_u32_e32 v15, vcc, 0, v45, vcc
	v_add_co_u32_e32 v16, vcc, s19, v44
	s_mov_b32 s20, 0x10000
	s_nop 0
	v_addc_co_u32_e32 v17, vcc, 0, v45, vcc
	v_add_co_u32_e32 v26, vcc, s20, v44
	s_mov_b32 s21, 0x14000
	s_nop 0
	v_addc_co_u32_e32 v27, vcc, 0, v45, vcc
	v_add_co_u32_e32 v28, vcc, s21, v44
	s_mov_b32 s22, 0x18000
	s_nop 0
	v_addc_co_u32_e32 v29, vcc, 0, v45, vcc
	v_add_co_u32_e32 v30, vcc, s22, v44
	s_mov_b32 s23, 0x1c000
	s_nop 0
	v_addc_co_u32_e32 v31, vcc, 0, v45, vcc
	v_add_co_u32_e32 v32, vcc, s23, v44
	s_mov_b32 s24, 0x20000
	s_nop 0
	v_addc_co_u32_e32 v33, vcc, 0, v45, vcc
	s_waitcnt vmcnt(34)
	v_add_co_u32_e32 v46, vcc, s24, v44
	s_mov_b32 s25, 0x24000
	s_waitcnt vmcnt(33)
	v_addc_co_u32_e32 v47, vcc, 0, v45, vcc
	s_waitcnt vmcnt(32)
	v_add_co_u32_e32 v48, vcc, s25, v44
	s_mov_b32 s26, 0x28000
	s_waitcnt vmcnt(31)
	v_addc_co_u32_e32 v49, vcc, 0, v45, vcc
	global_load_dwordx4 v[2:5], v[44:45], off nt
	global_load_dwordx4 v[6:9], v[10:11], off nt
	s_nop 0
	global_load_dwordx4 v[10:13], v[14:15], off nt
	global_load_dwordx4 v[18:21], v[16:17], off nt
	s_nop 0
	global_load_dwordx4 v[14:17], v[26:27], off nt
	global_load_dwordx4 v[22:25], v[28:29], off nt
	s_nop 0
	global_load_dwordx4 v[26:29], v[30:31], off nt
	global_load_dwordx4 v[34:37], v[32:33], off nt
	s_nop 0
	global_load_dwordx4 v[30:33], v[46:47], off nt
	global_load_dwordx4 v[38:41], v[48:49], off nt
	v_add_co_u32_e32 v46, vcc, s26, v44
	s_mov_b32 s27, 0x2c000
	s_nop 0
	v_addc_co_u32_e32 v47, vcc, 0, v45, vcc
	v_add_co_u32_e32 v48, vcc, s27, v44
	s_mov_b32 s28, 0x30000
	s_nop 0
	v_addc_co_u32_e32 v49, vcc, 0, v45, vcc
	global_load_dwordx4 v[54:57], v[46:47], off nt
	global_load_dwordx4 v[62:65], v[48:49], off nt
	v_add_co_u32_e32 v46, vcc, s28, v44
	s_mov_b32 s29, 0x34000
	s_nop 0
	v_addc_co_u32_e32 v47, vcc, 0, v45, vcc
	v_add_co_u32_e32 v48, vcc, s29, v44
	v_or_b32_e32 v42, 64, v42
	s_nop 0
	v_addc_co_u32_e32 v49, vcc, 0, v45, vcc
	s_mov_b32 s30, 0x38000
	v_ashrrev_i32_e32 v43, 31, v42
	global_load_dwordx4 v[50:53], v[46:47], off nt
	global_load_dwordx4 v[58:61], v[48:49], off nt
	v_add_co_u32_e32 v46, vcc, s30, v44
	v_lshlrev_b64 v[42:43], 14, v[42:43]
	s_nop 0
	v_addc_co_u32_e32 v47, vcc, 0, v45, vcc
	s_mov_b32 s31, 0x3c000
	v_lshl_add_u64 v[42:43], s[0:1], 0, v[42:43]
	v_add_co_u32_e32 v44, vcc, s31, v44
	v_lshl_add_u64 v[42:43], v[42:43], 0, s[2:3]
	s_nop 0
	v_addc_co_u32_e32 v45, vcc, 0, v45, vcc
	s_waitcnt vmcnt(31)
	v_lshl_add_u64 v[122:123], v[42:43], 0, v[132:133]
	global_load_dwordx4 v[82:85], v[46:47], off nt
	global_load_dwordx4 v[90:93], v[44:45], off nt
	v_add_co_u32_e32 v46, vcc, s11, v122
	s_movk_i32 s0, 0x410
	s_nop 0
	v_addc_co_u32_e32 v47, vcc, 0, v123, vcc
	s_waitcnt vmcnt(30)
	v_add_co_u32_e32 v66, vcc, s18, v122
	global_load_dwordx4 v[42:45], v[122:123], off nt
	s_nop 0
	global_load_dwordx4 v[46:49], v[46:47], off nt
	s_waitcnt vmcnt(31)
	v_addc_co_u32_e32 v67, vcc, 0, v123, vcc
	s_waitcnt vmcnt(30)
	v_add_co_u32_e32 v68, vcc, s19, v122
	v_mov_b32_e32 v141, s6
	s_waitcnt vmcnt(27)
	v_addc_co_u32_e32 v69, vcc, 0, v123, vcc
	global_load_dwordx4 v[70:73], v[66:67], off nt
	global_load_dwordx4 v[78:81], v[68:69], off nt
	v_add_co_u32_e32 v66, vcc, s20, v122
	v_lshlrev_b32_e32 v130, 2, v1
	s_nop 0
	v_addc_co_u32_e32 v67, vcc, 0, v123, vcc
	s_waitcnt vmcnt(24)
	v_add_co_u32_e32 v74, vcc, s21, v122
	v_add_u32_e32 v134, s6, v137
	s_nop 0
	v_addc_co_u32_e32 v75, vcc, 0, v123, vcc
	v_add_co_u32_e32 v86, vcc, s22, v122
	global_load_dwordx4 v[66:69], v[66:67], off nt
	s_nop 0
	global_load_dwordx4 v[74:77], v[74:75], off nt
	v_addc_co_u32_e32 v87, vcc, 0, v123, vcc
	v_add_co_u32_e32 v94, vcc, s23, v122
	v_add_u32_e32 v135, s6, v132
	s_nop 0
	v_addc_co_u32_e32 v95, vcc, 0, v123, vcc
	global_load_dwordx4 v[86:89], v[86:87], off nt
	s_nop 0
	global_load_dwordx4 v[98:101], v[94:95], off nt
	v_add_co_u32_e32 v94, vcc, s24, v122
	v_lshlrev_b32_e32 v139, 3, v198
	s_nop 0
	v_addc_co_u32_e32 v95, vcc, 0, v123, vcc
	v_add_co_u32_e32 v102, vcc, s25, v122
	v_mul_u32_u24_e32 v140, 0x410, v1
	s_nop 0
	v_addc_co_u32_e32 v103, vcc, 0, v123, vcc
	v_add_co_u32_e32 v106, vcc, s26, v122
	global_load_dwordx4 v[94:97], v[94:95], off nt
	s_nop 0
	global_load_dwordx4 v[102:105], v[102:103], off nt
	v_addc_co_u32_e32 v107, vcc, 0, v123, vcc
	v_add_co_u32_e32 v108, vcc, s27, v122
	v_mad_u32_u24 v142, v1, s0, v141
	s_nop 0
	v_addc_co_u32_e32 v109, vcc, 0, v123, vcc
	global_load_dwordx4 v[110:113], v[106:107], off nt
	global_load_dwordx4 v[118:121], v[108:109], off nt
	v_add_co_u32_e32 v106, vcc, s28, v122
	v_mul_u32_u24_e32 v141, 0x104, v136
	s_nop 0
	v_addc_co_u32_e32 v107, vcc, 0, v123, vcc
	v_add_co_u32_e32 v114, vcc, s29, v122
	v_or_b32_e32 v138, 64, v137
	s_nop 0
	v_addc_co_u32_e32 v115, vcc, 0, v123, vcc
	v_add_co_u32_e32 v124, vcc, s30, v122
	global_load_dwordx4 v[106:109], v[106:107], off nt
	s_nop 0
	global_load_dwordx4 v[114:117], v[114:115], off nt
	v_addc_co_u32_e32 v125, vcc, 0, v123, vcc
	v_add_co_u32_e32 v126, vcc, s31, v122
	v_and_b32_e32 v139, 0x80, v139
	s_nop 0
	v_addc_co_u32_e32 v127, vcc, 0, v123, vcc
	global_load_dwordx4 v[122:125], v[124:125], off nt
	s_nop 0
	global_load_dwordx4 v[126:129], v[126:127], off nt
	s_lshl_b32 s35, s34, 6
	s_lshl_b32 s33, s85, 6
	v_add_u32_e32 v140, v134, v140
	v_lshlrev_b32_e32 v130, 2, v130
	v_add_u32_e32 v141, v135, v141
	v_add_u32_e32 v142, v142, v137
	s_branch .LBB0_221

.LBB0_221:
	s_waitcnt vmcnt(31)
	v_mul_f32_e32 v134, 0x42800000, v2
	s_waitcnt vmcnt(30)
	v_mul_f32_e32 v6, 0x42800000, v6
	v_mov_b32_e32 v2, v131
	v_cvt_pk_fp8_f32 v2, v134, v6
	v_mul_f32_e32 v3, 0x42800000, v3
	v_mul_f32_e32 v6, 0x42800000, v7
	v_mov_b32_e32 v7, v131
	v_cvt_pk_fp8_f32 v7, v3, v6
	s_waitcnt vmcnt(29)
	v_mul_f32_e32 v3, 0x42800000, v11
	s_waitcnt vmcnt(28)
	v_mul_f32_e32 v6, 0x42800000, v19
	v_mul_f32_e32 v10, 0x42800000, v10
	v_cvt_pk_fp8_f32 v7, v3, v6 op_sel:[0,0,1]
	v_mul_f32_e32 v3, 0x42800000, v4
	v_mul_f32_e32 v4, 0x42800000, v8
	v_mov_b32_e32 v6, v131
	v_cvt_pk_fp8_f32 v6, v3, v4
	v_mul_f32_e32 v18, 0x42800000, v18
	v_mul_f32_e32 v3, 0x42800000, v5
	v_mul_f32_e32 v4, 0x42800000, v9
	v_mov_b32_e32 v5, v131
	v_cvt_pk_fp8_f32 v2, v10, v18 op_sel:[0,0,1]
	v_mul_f32_e32 v8, 0x42800000, v12
	v_mul_f32_e32 v10, 0x42800000, v20
	v_cvt_pk_fp8_f32 v5, v3, v4
	v_cvt_pk_fp8_f32 v6, v8, v10 op_sel:[0,0,1]
	s_waitcnt vmcnt(27)
	v_mul_f32_e32 v9, 0x42800000, v15
	s_waitcnt vmcnt(26)
	v_mul_f32_e32 v10, 0x42800000, v23
	v_mov_b32_e32 v11, v131
	v_cvt_pk_fp8_f32 v11, v9, v10
	v_mul_f32_e32 v3, 0x42800000, v13
	v_mul_f32_e32 v4, 0x42800000, v21
	v_cvt_pk_fp8_f32 v5, v3, v4 op_sel:[0,0,1]
	v_mul_f32_e32 v4, 0x42800000, v14
	v_mul_f32_e32 v8, 0x42800000, v22
	v_mov_b32_e32 v3, v131
	v_cvt_pk_fp8_f32 v3, v4, v8
	s_waitcnt vmcnt(25)
	v_mul_f32_e32 v4, 0x42800000, v27
	s_waitcnt vmcnt(24)
	v_mul_f32_e32 v8, 0x42800000, v35
	v_cvt_pk_fp8_f32 v11, v4, v8 op_sel:[0,0,1]
	v_mul_f32_e32 v9, 0x42800000, v17
	v_mul_f32_e32 v10, 0x42800000, v25
	v_mul_f32_e32 v4, 0x42800000, v26
	ds_write2_b32 v140, v7, v11 offset0:65 offset1:66
	v_mov_b32_e32 v11, v131
	v_cvt_pk_fp8_f32 v11, v9, v10
	v_mul_f32_e32 v8, 0x42800000, v34
	v_cvt_pk_fp8_f32 v3, v4, v8 op_sel:[0,0,1]
	v_mul_f32_e32 v4, 0x42800000, v16
	v_mul_f32_e32 v8, 0x42800000, v24
	v_mov_b32_e32 v7, v131
	v_cvt_pk_fp8_f32 v7, v4, v8
	v_mul_f32_e32 v4, 0x42800000, v29
	v_mul_f32_e32 v8, 0x42800000, v37
	v_cvt_pk_fp8_f32 v11, v4, v8 op_sel:[0,0,1]
	v_mul_f32_e32 v4, 0x42800000, v28
	v_mul_f32_e32 v8, 0x42800000, v36
	v_cvt_pk_fp8_f32 v7, v4, v8 op_sel:[0,0,1]
	ds_write2_b32 v140, v5, v11 offset0:195 offset1:196
	s_waitcnt vmcnt(23)
	v_mul_f32_e32 v5, 0x42800000, v30
	s_waitcnt vmcnt(22)
	v_mul_f32_e32 v8, 0x42800000, v38
	v_mov_b32_e32 v4, v131
	v_cvt_pk_fp8_f32 v4, v5, v8
	v_mul_f32_e32 v5, 0x42800000, v31
	v_mul_f32_e32 v8, 0x42800000, v39
	v_mov_b32_e32 v11, v131
	v_cvt_pk_fp8_f32 v11, v5, v8
	s_mov_b32 s4, s34
	s_waitcnt vmcnt(21)
	v_mul_f32_e32 v9, 0x42800000, v54
	s_waitcnt vmcnt(20)
	v_mul_f32_e32 v10, 0x42800000, v62
	v_mul_f32_e32 v5, 0x42800000, v55
	v_mul_f32_e32 v8, 0x42800000, v63
	v_cvt_pk_fp8_f32 v4, v9, v10 op_sel:[0,0,1]
	v_cvt_pk_fp8_f32 v11, v5, v8 op_sel:[0,0,1]
	v_mul_f32_e32 v5, 0x42800000, v32
	v_mul_f32_e32 v9, 0x42800000, v40
	v_mov_b32_e32 v8, v131
	s_ashr_i32 s0, s4, 31
	v_cvt_pk_fp8_f32 v8, v5, v9
	v_mul_f32_e32 v5, 0x42800000, v33
	v_mul_f32_e32 v9, 0x42800000, v41
	v_mov_b32_e32 v13, v131
	s_lshr_b32 s0, s0, 23
	v_cvt_pk_fp8_f32 v13, v5, v9
	s_add_i32 s5, s4, s0
	s_ashr_i32 s0, s5, 9
	s_ashr_i32 s1, s0, 31
	s_add_i32 s34, s34, s85
	v_mul_f32_e32 v10, 0x42800000, v56
	v_mul_f32_e32 v12, 0x42800000, v64
	v_mul_f32_e32 v5, 0x42800000, v57
	v_mul_f32_e32 v9, 0x42800000, v65
	s_lshl_b64 s[2:3], s[0:1], 25
	v_cvt_pk_fp8_f32 v8, v10, v12 op_sel:[0,0,1]
	v_cvt_pk_fp8_f32 v13, v5, v9 op_sel:[0,0,1]
	s_waitcnt vmcnt(19)
	v_mul_f32_e32 v9, 0x42800000, v50
	s_waitcnt vmcnt(18)
	v_mul_f32_e32 v10, 0x42800000, v58
	v_mov_b32_e32 v5, v131
	s_add_u32 s2, s16, s2
	v_cvt_pk_fp8_f32 v5, v9, v10
	v_mul_f32_e32 v9, 0x42800000, v51
	v_mul_f32_e32 v10, 0x42800000, v59
	v_mov_b32_e32 v15, v131
	s_addc_u32 s3, s17, s3
	s_and_b32 s5, s5, 0x7fe00
	v_cvt_pk_fp8_f32 v15, v9, v10
	s_sub_i32 s4, s4, s5
	s_lshr_b32 s4, s4, 3
	s_bfe_i32 s5, s4, 0x80000
	s_waitcnt vmcnt(17)
	v_mul_f32_e32 v12, 0x42800000, v82
	s_waitcnt vmcnt(16)
	v_mul_f32_e32 v14, 0x42800000, v90
	v_mul_f32_e32 v9, 0x42800000, v83
	v_mul_f32_e32 v10, 0x42800000, v91
	s_bfe_u32 s5, s5, 0x2000d
	v_cvt_pk_fp8_f32 v5, v12, v14 op_sel:[0,0,1]
	v_cvt_pk_fp8_f32 v15, v9, v10 op_sel:[0,0,1]
	v_mul_f32_e32 v10, 0x42800000, v52
	v_mul_f32_e32 v12, 0x42800000, v60
	v_mov_b32_e32 v9, v131
	s_add_i32 s5, s4, s5
	v_cvt_pk_fp8_f32 v9, v10, v12
	v_mul_f32_e32 v10, 0x42800000, v53
	v_mul_f32_e32 v12, 0x42800000, v61
	v_mov_b32_e32 v17, v131
	s_bfe_i32 s8, s5, 0x80000
	s_and_b32 s5, s5, 0xfc
	v_cvt_pk_fp8_f32 v17, v10, v12
	s_sub_i32 s4, s4, s5
	s_lshl_b32 s38, s0, 15
	s_sext_i32_i8 s4, s4
	s_sub_i32 s5, s35, s38
	v_mul_f32_e32 v14, 0x42800000, v84
	v_mul_f32_e32 v16, 0x42800000, v92
	s_lshl_b32 s4, s4, 9
	s_and_b32 s9, s5, 0x100
	v_cvt_pk_fp8_f32 v9, v14, v16 op_sel:[0,0,1]
	v_mul_f32_e32 v10, 0x42800000, v85
	v_mul_f32_e32 v12, 0x42800000, v93
	s_sext_i32_i16 s8, s8
	s_or_b32 s37, s4, s9
	v_cvt_pk_fp8_f32 v17, v10, v12 op_sel:[0,0,1]
	v_or_b32_e32 v134, s37, v137
	s_lshl_b32 s4, s8, 6
	ds_write_b128 v140, v[2:5]
	ds_write2_b32 v140, v11, v15 offset0:67 offset1:68
	ds_write2_b64 v140, v[6:7], v[8:9] offset0:65 offset1:66
	ds_write2_b32 v140, v13, v17 offset0:197 offset1:198
	v_or_b32_e32 v2, 0x80, v134
	s_and_b32 s36, s4, 0xffffff00
	s_and_b32 s4, s5, 0xc0
	v_ashrrev_i32_e32 v3, 31, v2
	s_or_b32 s4, s36, s4
	v_lshlrev_b64 v[2:3], 14, v[2:3]
	s_ashr_i32 s5, s4, 31
	v_lshl_add_u64 v[2:3], s[2:3], 0, v[2:3]
	s_lshl_b64 s[4:5], s[4:5], 2
	v_lshl_add_u64 v[2:3], v[2:3], 0, s[4:5]
	v_lshl_add_u64 v[82:83], v[2:3], 0, v[130:131]
	v_add_co_u32_e32 v6, vcc, s11, v82
	s_waitcnt vmcnt(15)
	v_mul_f32_e32 v135, 0x42800000, v42
	v_addc_co_u32_e32 v7, vcc, 0, v83, vcc
	v_add_co_u32_e32 v10, vcc, s18, v82
	global_load_dwordx4 v[2:5], v[82:83], off nt
	s_nop 0
	global_load_dwordx4 v[6:9], v[6:7], off nt
	v_addc_co_u32_e32 v11, vcc, 0, v83, vcc
	v_add_co_u32_e32 v14, vcc, s19, v82
	s_waitcnt vmcnt(16)
	v_mul_f32_e32 v46, 0x42800000, v46
	v_addc_co_u32_e32 v15, vcc, 0, v83, vcc
	global_load_dwordx4 v[10:13], v[10:11], off nt
	s_nop 0
	global_load_dwordx4 v[18:21], v[14:15], off nt
	v_add_co_u32_e32 v14, vcc, s20, v82
	v_mov_b32_e32 v42, v131
	s_nop 0
	v_addc_co_u32_e32 v15, vcc, 0, v83, vcc
	v_add_co_u32_e32 v22, vcc, s21, v82
	v_cvt_pk_fp8_f32 v42, v135, v46
	s_nop 0
	v_addc_co_u32_e32 v23, vcc, 0, v83, vcc
	v_add_co_u32_e32 v26, vcc, s22, v82
	v_mul_f32_e32 v43, 0x42800000, v43
	v_mul_f32_e32 v46, 0x42800000, v47
	v_mov_b32_e32 v47, v131
	v_addc_co_u32_e32 v27, vcc, 0, v83, vcc
	v_cvt_pk_fp8_f32 v47, v43, v46
	v_add_co_u32_e32 v30, vcc, s23, v82
	global_load_dwordx4 v[14:17], v[14:15], off nt
	s_nop 0
	global_load_dwordx4 v[22:25], v[22:23], off nt
	v_addc_co_u32_e32 v31, vcc, 0, v83, vcc
	global_load_dwordx4 v[26:29], v[26:27], off nt
	s_nop 0
	global_load_dwordx4 v[34:37], v[30:31], off nt
	v_add_co_u32_e32 v30, vcc, s24, v82
	s_waitcnt vmcnt(21)
	v_mul_f32_e32 v43, 0x42800000, v71
	s_waitcnt vmcnt(20)
	v_mul_f32_e32 v46, 0x42800000, v79
	v_addc_co_u32_e32 v31, vcc, 0, v83, vcc
	v_cvt_pk_fp8_f32 v47, v43, v46 op_sel:[0,0,1]
	v_mul_f32_e32 v43, 0x42800000, v44
	v_mul_f32_e32 v44, 0x42800000, v48
	v_mov_b32_e32 v46, v131
	v_add_co_u32_e32 v38, vcc, s25, v82
	v_cvt_pk_fp8_f32 v46, v43, v44
	v_mul_f32_e32 v43, 0x42800000, v45
	v_mul_f32_e32 v44, 0x42800000, v49
	v_mov_b32_e32 v45, v131
	v_addc_co_u32_e32 v39, vcc, 0, v83, vcc
	v_cvt_pk_fp8_f32 v45, v43, v44
	v_add_co_u32_e32 v50, vcc, s26, v82
	v_mul_f32_e32 v43, 0x42800000, v73
	s_nop 0
	v_addc_co_u32_e32 v51, vcc, 0, v83, vcc
	v_add_co_u32_e32 v52, vcc, s27, v82
	v_mul_f32_e32 v44, 0x42800000, v81
	s_nop 0
	v_addc_co_u32_e32 v53, vcc, 0, v83, vcc
	v_cvt_pk_fp8_f32 v45, v43, v44 op_sel:[0,0,1]
	s_waitcnt vmcnt(19)
	v_mul_f32_e32 v44, 0x42800000, v66
	v_mul_f32_e32 v49, 0x42800000, v67
	s_waitcnt vmcnt(18)
	v_mul_f32_e32 v66, 0x42800000, v75
	v_mov_b32_e32 v67, v131
	global_load_dwordx4 v[30:33], v[30:31], off nt
	s_nop 0
	global_load_dwordx4 v[38:41], v[38:39], off nt
	s_nop 0
	global_load_dwordx4 v[54:57], v[50:51], off nt
	global_load_dwordx4 v[62:65], v[52:53], off nt
	v_add_co_u32_e32 v50, vcc, s28, v82
	v_mul_f32_e32 v70, 0x42800000, v70
	v_mul_f32_e32 v78, 0x42800000, v78
	v_cvt_pk_fp8_f32 v67, v49, v66
	v_addc_co_u32_e32 v51, vcc, 0, v83, vcc
	v_cvt_pk_fp8_f32 v42, v70, v78 op_sel:[0,0,1]
	v_mul_f32_e32 v48, 0x42800000, v72
	v_mul_f32_e32 v70, 0x42800000, v80
	v_add_co_u32_e32 v58, vcc, s29, v82
	v_cvt_pk_fp8_f32 v46, v48, v70 op_sel:[0,0,1]
	v_mul_f32_e32 v48, 0x42800000, v74
	v_mov_b32_e32 v43, v131
	v_addc_co_u32_e32 v59, vcc, 0, v83, vcc
	v_cvt_pk_fp8_f32 v43, v44, v48
	s_waitcnt vmcnt(21)
	v_mul_f32_e32 v44, 0x42800000, v87
	s_waitcnt vmcnt(20)
	v_mul_f32_e32 v48, 0x42800000, v99
	v_add_co_u32_e32 v84, vcc, s30, v82
	v_cvt_pk_fp8_f32 v67, v44, v48 op_sel:[0,0,1]
	s_nop 0
	v_addc_co_u32_e32 v85, vcc, 0, v83, vcc
	v_add_co_u32_e32 v90, vcc, s31, v82
	global_load_dwordx4 v[50:53], v[50:51], off nt
	s_nop 0
	global_load_dwordx4 v[58:61], v[58:59], off nt
	v_addc_co_u32_e32 v91, vcc, 0, v83, vcc
	global_load_dwordx4 v[82:85], v[84:85], off nt
	s_nop 0
	global_load_dwordx4 v[90:93], v[90:91], off nt
	ds_write2_b32 v142, v47, v67 offset0:81 offset1:82
	v_mul_f32_e32 v49, 0x42800000, v69
	v_mul_f32_e32 v66, 0x42800000, v77
	v_mov_b32_e32 v67, v131
	v_cvt_pk_fp8_f32 v67, v49, v66
	v_mul_f32_e32 v44, 0x42800000, v86
	v_mul_f32_e32 v48, 0x42800000, v98
	v_cvt_pk_fp8_f32 v43, v44, v48 op_sel:[0,0,1]
	v_mul_f32_e32 v44, 0x42800000, v68
	v_mul_f32_e32 v48, 0x42800000, v76
	v_mov_b32_e32 v47, v131
	v_cvt_pk_fp8_f32 v47, v44, v48
	v_mul_f32_e32 v44, 0x42800000, v89
	v_mul_f32_e32 v48, 0x42800000, v101
	v_cvt_pk_fp8_f32 v67, v44, v48 op_sel:[0,0,1]
	v_mul_f32_e32 v44, 0x42800000, v88
	v_mul_f32_e32 v48, 0x42800000, v100
	v_cvt_pk_fp8_f32 v47, v44, v48 op_sel:[0,0,1]
	ds_write2_b32 v142, v45, v67 offset0:211 offset1:212
	s_waitcnt vmcnt(23)
	v_mul_f32_e32 v45, 0x42800000, v94
	s_waitcnt vmcnt(22)
	v_mul_f32_e32 v48, 0x42800000, v102
	v_mov_b32_e32 v44, v131
	v_cvt_pk_fp8_f32 v44, v45, v48
	v_mul_f32_e32 v45, 0x42800000, v95
	v_mul_f32_e32 v48, 0x42800000, v103
	v_mov_b32_e32 v67, v131
	v_cvt_pk_fp8_f32 v67, v45, v48
	s_waitcnt vmcnt(21)
	v_mul_f32_e32 v49, 0x42800000, v110
	s_waitcnt vmcnt(20)
	v_mul_f32_e32 v66, 0x42800000, v118
	v_mul_f32_e32 v45, 0x42800000, v111
	v_mul_f32_e32 v48, 0x42800000, v119
	v_cvt_pk_fp8_f32 v44, v49, v66 op_sel:[0,0,1]
	v_cvt_pk_fp8_f32 v67, v45, v48 op_sel:[0,0,1]
	v_mul_f32_e32 v45, 0x42800000, v96
	v_mul_f32_e32 v49, 0x42800000, v104
	v_mov_b32_e32 v48, v131
	v_cvt_pk_fp8_f32 v48, v45, v49
	v_mul_f32_e32 v45, 0x42800000, v97
	v_mul_f32_e32 v49, 0x42800000, v105
	v_mov_b32_e32 v69, v131
	v_cvt_pk_fp8_f32 v69, v45, v49
	v_mul_f32_e32 v66, 0x42800000, v112
	v_mul_f32_e32 v68, 0x42800000, v120
	v_mul_f32_e32 v45, 0x42800000, v113
	v_mul_f32_e32 v49, 0x42800000, v121
	v_cvt_pk_fp8_f32 v48, v66, v68 op_sel:[0,0,1]
	v_cvt_pk_fp8_f32 v69, v45, v49 op_sel:[0,0,1]
	s_waitcnt vmcnt(19)
	v_mul_f32_e32 v49, 0x42800000, v106
	s_waitcnt vmcnt(18)
	v_mul_f32_e32 v66, 0x42800000, v114
	v_mov_b32_e32 v45, v131
	v_cvt_pk_fp8_f32 v45, v49, v66
	v_mul_f32_e32 v49, 0x42800000, v107
	v_mul_f32_e32 v66, 0x42800000, v115
	v_mov_b32_e32 v71, v131
	v_cvt_pk_fp8_f32 v71, v49, v66
	s_waitcnt vmcnt(17)
	v_mul_f32_e32 v68, 0x42800000, v122
	s_waitcnt vmcnt(16)
	v_mul_f32_e32 v70, 0x42800000, v126
	v_mul_f32_e32 v49, 0x42800000, v123
	v_mul_f32_e32 v66, 0x42800000, v127
	v_cvt_pk_fp8_f32 v45, v68, v70 op_sel:[0,0,1]
	v_cvt_pk_fp8_f32 v71, v49, v66 op_sel:[0,0,1]
	v_mul_f32_e32 v66, 0x42800000, v108
	v_mul_f32_e32 v68, 0x42800000, v116
	v_mov_b32_e32 v49, v131
	v_cvt_pk_fp8_f32 v49, v66, v68
	v_mul_f32_e32 v66, 0x42800000, v109
	v_mul_f32_e32 v68, 0x42800000, v117
	v_mov_b32_e32 v73, v131
	v_cvt_pk_fp8_f32 v73, v66, v68
	v_mul_f32_e32 v70, 0x42800000, v124
	v_mul_f32_e32 v72, 0x42800000, v128
	v_cvt_pk_fp8_f32 v49, v70, v72 op_sel:[0,0,1]
	v_mul_f32_e32 v66, 0x42800000, v125
	v_mul_f32_e32 v68, 0x42800000, v129
	v_cvt_pk_fp8_f32 v73, v66, v68 op_sel:[0,0,1]
	ds_write_b128 v142, v[42:45] offset:64
	ds_write2_b32 v142, v67, v71 offset0:83 offset1:84
	ds_write2_b64 v142, v[46:47], v[48:49] offset0:73 offset1:74
	ds_write2_b32 v142, v69, v73 offset0:213 offset1:214
	v_or_b32_e32 v42, 0xc0, v134
	v_ashrrev_i32_e32 v43, 31, v42
	v_lshlrev_b64 v[42:43], 14, v[42:43]
	v_lshl_add_u64 v[42:43], s[2:3], 0, v[42:43]
	v_lshl_add_u64 v[42:43], v[42:43], 0, s[4:5]
	v_lshl_add_u64 v[122:123], v[42:43], 0, v[130:131]
	v_add_co_u32_e32 v46, vcc, s11, v122
	s_waitcnt vmcnt(15)
	v_mul_f32_e32 v134, 0x42800000, v2
	v_addc_co_u32_e32 v47, vcc, 0, v123, vcc
	v_add_co_u32_e32 v66, vcc, s18, v122
	global_load_dwordx4 v[42:45], v[122:123], off nt
	s_nop 0
	global_load_dwordx4 v[46:49], v[46:47], off nt
	v_addc_co_u32_e32 v67, vcc, 0, v123, vcc
	v_add_co_u32_e32 v68, vcc, s19, v122
	s_waitcnt vmcnt(16)
	v_mul_f32_e32 v135, 0x42800000, v6
	v_addc_co_u32_e32 v69, vcc, 0, v123, vcc
	global_load_dwordx4 v[70:73], v[66:67], off nt
	global_load_dwordx4 v[78:81], v[68:69], off nt
	v_add_co_u32_e32 v66, vcc, s20, v122
	v_mov_b32_e32 v144, v131
	s_nop 0
	v_addc_co_u32_e32 v67, vcc, 0, v123, vcc
	v_add_co_u32_e32 v74, vcc, s21, v122
	v_cvt_pk_fp8_f32 v144, v134, v135
	s_nop 0
	v_addc_co_u32_e32 v75, vcc, 0, v123, vcc
	v_add_co_u32_e32 v86, vcc, s22, v122
	global_load_dwordx4 v[66:69], v[66:67], off nt
	s_nop 0
	global_load_dwordx4 v[74:77], v[74:75], off nt
	v_addc_co_u32_e32 v87, vcc, 0, v123, vcc
	v_add_co_u32_e32 v94, vcc, s23, v122
	v_mul_f32_e32 v134, 0x42800000, v3
	s_nop 0
	v_addc_co_u32_e32 v95, vcc, 0, v123, vcc
	global_load_dwordx4 v[86:89], v[86:87], off nt
	s_nop 0
	global_load_dwordx4 v[98:101], v[94:95], off nt
	v_add_co_u32_e32 v94, vcc, s24, v122
	v_mul_f32_e32 v135, 0x42800000, v7
	s_nop 0
	v_addc_co_u32_e32 v95, vcc, 0, v123, vcc
	v_add_co_u32_e32 v102, vcc, s25, v122
	v_mov_b32_e32 v146, v131
	s_nop 0
	v_addc_co_u32_e32 v103, vcc, 0, v123, vcc
	v_add_co_u32_e32 v106, vcc, s26, v122
	global_load_dwordx4 v[94:97], v[94:95], off nt
	s_nop 0
	global_load_dwordx4 v[102:105], v[102:103], off nt
	v_addc_co_u32_e32 v107, vcc, 0, v123, vcc
	v_add_co_u32_e32 v108, vcc, s27, v122
	v_cvt_pk_fp8_f32 v146, v134, v135
	s_nop 0
	v_addc_co_u32_e32 v109, vcc, 0, v123, vcc
	global_load_dwordx4 v[110:113], v[106:107], off nt
	global_load_dwordx4 v[118:121], v[108:109], off nt
	v_add_co_u32_e32 v106, vcc, s28, v122
	s_waitcnt vmcnt(25)
	v_mul_f32_e32 v143, 0x42800000, v10
	v_addc_co_u32_e32 v107, vcc, 0, v123, vcc
	v_add_co_u32_e32 v114, vcc, s29, v122
	s_waitcnt vmcnt(24)
	v_mul_f32_e32 v145, 0x42800000, v18
	v_addc_co_u32_e32 v115, vcc, 0, v123, vcc
	v_add_co_u32_e32 v124, vcc, s30, v122
	global_load_dwordx4 v[106:109], v[106:107], off nt
	s_nop 0
	global_load_dwordx4 v[114:117], v[114:115], off nt
	v_addc_co_u32_e32 v125, vcc, 0, v123, vcc
	v_add_co_u32_e32 v126, vcc, s31, v122
	v_mul_f32_e32 v134, 0x42800000, v11
	s_nop 0
	v_addc_co_u32_e32 v127, vcc, 0, v123, vcc
	global_load_dwordx4 v[122:125], v[124:125], off nt
	s_nop 0
	global_load_dwordx4 v[126:129], v[126:127], off nt
	v_mul_f32_e32 v135, 0x42800000, v19
	v_cvt_pk_fp8_f32 v144, v143, v145 op_sel:[0,0,1]
	v_cvt_pk_fp8_f32 v146, v134, v135 op_sel:[0,0,1]
	v_mul_f32_e32 v135, 0x42800000, v4
	v_mul_f32_e32 v143, 0x42800000, v8
	v_mov_b32_e32 v134, v131
	v_cvt_pk_fp8_f32 v134, v135, v143
	v_mul_f32_e32 v135, 0x42800000, v5
	v_mul_f32_e32 v143, 0x42800000, v9
	v_mov_b32_e32 v148, v131
	v_mul_f32_e32 v145, 0x42800000, v12
	v_mul_f32_e32 v147, 0x42800000, v20
	v_cvt_pk_fp8_f32 v148, v135, v143
	v_cvt_pk_fp8_f32 v134, v145, v147 op_sel:[0,0,1]
	s_waitcnt vmcnt(27)
	v_mul_f32_e32 v147, 0x42800000, v15
	s_waitcnt vmcnt(26)
	v_mul_f32_e32 v149, 0x42800000, v23
	v_mov_b32_e32 v150, v131
	v_cvt_pk_fp8_f32 v150, v147, v149
	v_mul_f32_e32 v135, 0x42800000, v13
	v_mul_f32_e32 v143, 0x42800000, v21
	v_cvt_pk_fp8_f32 v148, v135, v143 op_sel:[0,0,1]
	v_mul_f32_e32 v135, 0x42800000, v14
	v_mul_f32_e32 v143, 0x42800000, v22
	v_mov_b32_e32 v145, v131
	v_cvt_pk_fp8_f32 v145, v135, v143
	s_waitcnt vmcnt(25)
	v_mul_f32_e32 v135, 0x42800000, v27
	s_waitcnt vmcnt(24)
	v_mul_f32_e32 v143, 0x42800000, v35
	v_cvt_pk_fp8_f32 v150, v135, v143 op_sel:[0,0,1]
	v_mul_f32_e32 v147, 0x42800000, v17
	v_mul_f32_e32 v149, 0x42800000, v25
	v_mul_f32_e32 v135, 0x42800000, v26
	ds_write2_b32 v142, v146, v150 offset0:97 offset1:98
	v_mov_b32_e32 v150, v131
	v_cvt_pk_fp8_f32 v150, v147, v149
	v_mul_f32_e32 v143, 0x42800000, v34
	v_cvt_pk_fp8_f32 v145, v135, v143 op_sel:[0,0,1]
	v_mul_f32_e32 v143, 0x42800000, v16
	v_mul_f32_e32 v146, 0x42800000, v24
	v_mov_b32_e32 v135, v131
	v_cvt_pk_fp8_f32 v135, v143, v146
	v_mul_f32_e32 v143, 0x42800000, v29
	v_mul_f32_e32 v146, 0x42800000, v37
	v_cvt_pk_fp8_f32 v150, v143, v146 op_sel:[0,0,1]
	v_mul_f32_e32 v143, 0x42800000, v28
	v_mul_f32_e32 v146, 0x42800000, v36
	v_cvt_pk_fp8_f32 v135, v143, v146 op_sel:[0,0,1]
	s_waitcnt vmcnt(23)
	v_mul_f32_e32 v143, 0x42800000, v30
	s_waitcnt vmcnt(22)
	v_mul_f32_e32 v147, 0x42800000, v38
	v_mov_b32_e32 v146, v131
	ds_write2_b32 v142, v148, v150 offset0:227 offset1:228
	v_cvt_pk_fp8_f32 v146, v143, v147
	v_mul_f32_e32 v143, 0x42800000, v31
	v_mul_f32_e32 v147, 0x42800000, v39
	v_mov_b32_e32 v150, v131
	v_cvt_pk_fp8_f32 v150, v143, v147
	s_waitcnt vmcnt(21)
	v_mul_f32_e32 v148, 0x42800000, v54
	s_waitcnt vmcnt(20)
	v_mul_f32_e32 v149, 0x42800000, v62
	v_mul_f32_e32 v143, 0x42800000, v55
	v_mul_f32_e32 v147, 0x42800000, v63
	v_cvt_pk_fp8_f32 v146, v148, v149 op_sel:[0,0,1]
	v_cvt_pk_fp8_f32 v150, v143, v147 op_sel:[0,0,1]
	v_mul_f32_e32 v143, 0x42800000, v32
	v_mul_f32_e32 v147, 0x42800000, v40
	v_mov_b32_e32 v148, v131
	v_cvt_pk_fp8_f32 v148, v143, v147
	v_mul_f32_e32 v143, 0x42800000, v33
	v_mul_f32_e32 v147, 0x42800000, v41
	v_mov_b32_e32 v152, v131
	v_cvt_pk_fp8_f32 v152, v143, v147
	v_mul_f32_e32 v149, 0x42800000, v56
	v_mul_f32_e32 v151, 0x42800000, v64
	v_mul_f32_e32 v143, 0x42800000, v57
	v_mul_f32_e32 v147, 0x42800000, v65
	v_cvt_pk_fp8_f32 v148, v149, v151 op_sel:[0,0,1]
	v_cvt_pk_fp8_f32 v152, v143, v147 op_sel:[0,0,1]
	s_waitcnt vmcnt(19)
	v_mul_f32_e32 v143, 0x42800000, v50
	s_waitcnt vmcnt(18)
	v_mul_f32_e32 v149, 0x42800000, v58
	v_mov_b32_e32 v147, v131
	v_cvt_pk_fp8_f32 v147, v143, v149
	v_mul_f32_e32 v143, 0x42800000, v51
	v_mul_f32_e32 v149, 0x42800000, v59
	v_mov_b32_e32 v154, v131
	v_cvt_pk_fp8_f32 v154, v143, v149
	s_waitcnt vmcnt(17)
	v_mul_f32_e32 v151, 0x42800000, v82
	s_waitcnt vmcnt(16)
	v_mul_f32_e32 v153, 0x42800000, v90
	v_mul_f32_e32 v143, 0x42800000, v83
	v_mul_f32_e32 v149, 0x42800000, v91
	v_cvt_pk_fp8_f32 v147, v151, v153 op_sel:[0,0,1]
	v_cvt_pk_fp8_f32 v154, v143, v149 op_sel:[0,0,1]
	v_mul_f32_e32 v143, 0x42800000, v52
	v_mul_f32_e32 v151, 0x42800000, v60
	v_mov_b32_e32 v149, v131
	v_cvt_pk_fp8_f32 v149, v143, v151
	v_mul_f32_e32 v143, 0x42800000, v53
	v_mul_f32_e32 v151, 0x42800000, v61
	v_mov_b32_e32 v156, v131
	v_cvt_pk_fp8_f32 v156, v143, v151
	v_mul_f32_e32 v153, 0x42800000, v84
	v_mul_f32_e32 v155, 0x42800000, v92
	s_cmpk_gt_i32 s34, 0x3fff
	v_cvt_pk_fp8_f32 v149, v153, v155 op_sel:[0,0,1]
	v_mul_f32_e32 v143, 0x42800000, v85
	v_mul_f32_e32 v151, 0x42800000, v93
	s_cselect_b64 s[2:3], -1, 0
	v_cvt_pk_fp8_f32 v156, v143, v151 op_sel:[0,0,1]
	s_and_b64 vcc, exec, s[2:3]
	ds_write_b128 v142, v[144:147] offset:128
	ds_write2_b32 v142, v150, v154 offset0:99 offset1:100
	ds_write2_b64 v142, v[134:135], v[148:149] offset0:81 offset1:82
	ds_write2_b32 v142, v152, v156 offset0:229 offset1:230
	s_cbranch_vccnz .LBB0_223
	s_ashr_i32 s4, s34, 31
	s_lshr_b32 s4, s4, 23
	s_add_i32 s8, s34, s4
	s_ashr_i32 s4, s8, 9
	s_ashr_i32 s5, s4, 31
	s_lshl_b64 s[4:5], s[4:5], 25
	s_add_u32 s4, s16, s4
	s_addc_u32 s5, s17, s5
	s_and_b32 s8, s8, 0xfffffe00
	s_sub_i32 s8, s34, s8
	s_lshr_b32 s9, s8, 3
	s_bfe_i32 s39, s9, 0x80000
	s_bfe_u32 s39, s39, 0x2000d
	s_add_i32 s39, s9, s39
	s_bfe_i32 s40, s39, 0x80000
	s_and_b32 s39, s39, 0xfc
	s_sub_i32 s9, s9, s39
	s_sext_i32_i8 s9, s9
	s_lshl_b32 s8, s8, 6
	s_lshl_b32 s9, s9, 9
	s_and_b32 s39, s8, 0x100
	s_or_b32 s9, s9, s39
	v_or_b32_e32 v2, s9, v137
	v_ashrrev_i32_e32 v3, 31, v2
	s_sext_i32_i16 s40, s40
	v_lshlrev_b64 v[2:3], 14, v[2:3]
	v_lshl_add_u64 v[2:3], s[4:5], 0, v[2:3]
	s_lshl_b32 s4, s40, 6
	s_and_b32 s4, s4, 0xffffff00
	s_and_b32 s5, s8, 0xc0
	s_or_b32 s4, s4, s5
	s_ashr_i32 s5, s4, 31
	v_lshl_add_u64 v[2:3], s[4:5], 2, v[2:3]
	v_lshl_add_u64 v[82:83], v[2:3], 0, v[130:131]
	v_add_co_u32_e32 v6, vcc, s11, v82
	s_nop 1
	v_addc_co_u32_e32 v7, vcc, 0, v83, vcc
	v_add_co_u32_e32 v10, vcc, s18, v82
	global_load_dwordx4 v[2:5], v[82:83], off nt
	s_nop 0
	global_load_dwordx4 v[6:9], v[6:7], off nt
	v_addc_co_u32_e32 v11, vcc, 0, v83, vcc
	v_add_co_u32_e32 v14, vcc, s19, v82
	s_nop 1
	v_addc_co_u32_e32 v15, vcc, 0, v83, vcc
	global_load_dwordx4 v[10:13], v[10:11], off nt
	s_nop 0
	global_load_dwordx4 v[18:21], v[14:15], off nt
	v_add_co_u32_e32 v14, vcc, s20, v82
	s_nop 1
	v_addc_co_u32_e32 v15, vcc, 0, v83, vcc
	v_add_co_u32_e32 v22, vcc, s21, v82
	s_nop 1
	v_addc_co_u32_e32 v23, vcc, 0, v83, vcc
	v_add_co_u32_e32 v26, vcc, s22, v82
	global_load_dwordx4 v[14:17], v[14:15], off nt
	s_nop 0
	global_load_dwordx4 v[22:25], v[22:23], off nt
	v_addc_co_u32_e32 v27, vcc, 0, v83, vcc
	v_add_co_u32_e32 v30, vcc, s23, v82
	s_nop 1
	v_addc_co_u32_e32 v31, vcc, 0, v83, vcc
	global_load_dwordx4 v[26:29], v[26:27], off nt
	s_nop 0
	global_load_dwordx4 v[34:37], v[30:31], off nt
	v_add_co_u32_e32 v30, vcc, s24, v82
	s_nop 1
	v_addc_co_u32_e32 v31, vcc, 0, v83, vcc
	v_add_co_u32_e32 v38, vcc, s25, v82
	s_nop 1
	v_addc_co_u32_e32 v39, vcc, 0, v83, vcc
	v_add_co_u32_e32 v50, vcc, s26, v82
	global_load_dwordx4 v[30:33], v[30:31], off nt
	s_nop 0
	global_load_dwordx4 v[38:41], v[38:39], off nt
	v_addc_co_u32_e32 v51, vcc, 0, v83, vcc
	v_add_co_u32_e32 v52, vcc, s27, v82
	s_nop 1
	v_addc_co_u32_e32 v53, vcc, 0, v83, vcc
	global_load_dwordx4 v[54:57], v[50:51], off nt
	global_load_dwordx4 v[62:65], v[52:53], off nt
	v_add_co_u32_e32 v50, vcc, 0x30000, v82
	s_nop 1
	v_addc_co_u32_e32 v51, vcc, 0, v83, vcc
	v_add_co_u32_e32 v58, vcc, 0x34000, v82
	s_nop 1
	v_addc_co_u32_e32 v59, vcc, 0, v83, vcc
	v_add_co_u32_e32 v84, vcc, 0x38000, v82
	global_load_dwordx4 v[50:53], v[50:51], off nt
	s_nop 0
	global_load_dwordx4 v[58:61], v[58:59], off nt
	v_addc_co_u32_e32 v85, vcc, 0, v83, vcc
	v_add_co_u32_e32 v90, vcc, 0x3c000, v82
	s_nop 1
	v_addc_co_u32_e32 v91, vcc, 0, v83, vcc
	global_load_dwordx4 v[82:85], v[84:85], off nt
	s_nop 0
	global_load_dwordx4 v[90:93], v[90:91], off nt

.LBB0_225:
	s_lshl_b64 s[0:1], s[0:1], 23
	s_andn2_b64 vcc, exec, s[2:3]
	s_sub_i32 s2, 0, s38
	s_cbranch_vccnz .LBB0_220
	s_ashr_i32 s3, s34, 31
	s_lshr_b32 s3, s3, 23
	s_add_i32 s3, s34, s3
	s_ashr_i32 s38, s3, 9
	s_ashr_i32 s39, s38, 31
	s_lshl_b64 s[4:5], s[38:39], 25
	s_add_u32 s40, s16, s4
	s_addc_u32 s41, s17, s5
	s_and_b32 s3, s3, 0x7fe00
	s_sub_i32 s3, s34, s3
	s_lshr_b32 s3, s3, 3
	s_bfe_i32 s4, s3, 0x80000
	s_bfe_u32 s4, s4, 0x2000d
	s_add_i32 s4, s3, s4
	s_bfe_i32 s5, s4, 0x80000
	s_and_b32 s4, s4, 0xfc
	s_sub_i32 s3, s3, s4
	s_add_i32 s4, s33, s35
	s_lshl_b32 s38, s38, 15
	s_sext_i32_i8 s3, s3
	s_sub_i32 s38, s4, s38
	s_lshl_b32 s3, s3, 9
	s_and_b32 s39, s38, 0x100
	s_sext_i32_i16 s5, s5
	s_or_b32 s3, s3, s39
	v_or_b32_e32 v42, s3, v138
	s_lshl_b32 s3, s5, 6
	v_ashrrev_i32_e32 v43, 31, v42
	s_and_b32 s3, s3, 0xffffff00
	s_and_b32 s5, s38, 0xc0
	v_lshlrev_b64 v[42:43], 14, v[42:43]
	s_or_b32 s38, s3, s5
	v_lshl_add_u64 v[42:43], s[40:41], 0, v[42:43]
	s_ashr_i32 s39, s38, 31
	v_lshl_add_u64 v[42:43], s[38:39], 2, v[42:43]
	v_lshl_add_u64 v[122:123], v[42:43], 0, v[130:131]
	v_add_co_u32_e32 v46, vcc, s11, v122
	s_nop 1
	v_addc_co_u32_e32 v47, vcc, 0, v123, vcc
	v_add_co_u32_e32 v66, vcc, s18, v122
	global_load_dwordx4 v[42:45], v[122:123], off nt
	s_nop 0
	global_load_dwordx4 v[46:49], v[46:47], off nt
	v_addc_co_u32_e32 v67, vcc, 0, v123, vcc
	v_add_co_u32_e32 v68, vcc, s19, v122
	s_nop 1
	v_addc_co_u32_e32 v69, vcc, 0, v123, vcc
	global_load_dwordx4 v[70:73], v[66:67], off nt
	global_load_dwordx4 v[78:81], v[68:69], off nt
	v_add_co_u32_e32 v66, vcc, s20, v122
	s_nop 1
	v_addc_co_u32_e32 v67, vcc, 0, v123, vcc
	v_add_co_u32_e32 v74, vcc, s21, v122
	s_nop 1
	v_addc_co_u32_e32 v75, vcc, 0, v123, vcc
	v_add_co_u32_e32 v86, vcc, s22, v122
	global_load_dwordx4 v[66:69], v[66:67], off nt
	s_nop 0
	global_load_dwordx4 v[74:77], v[74:75], off nt
	v_addc_co_u32_e32 v87, vcc, 0, v123, vcc
	v_add_co_u32_e32 v94, vcc, s23, v122
	s_nop 1
	v_addc_co_u32_e32 v95, vcc, 0, v123, vcc
	global_load_dwordx4 v[86:89], v[86:87], off nt
	s_nop 0
	global_load_dwordx4 v[98:101], v[94:95], off nt
	v_add_co_u32_e32 v94, vcc, s24, v122
	s_nop 1
	v_addc_co_u32_e32 v95, vcc, 0, v123, vcc
	v_add_co_u32_e32 v102, vcc, s25, v122
	s_nop 1
	v_addc_co_u32_e32 v103, vcc, 0, v123, vcc
	v_add_co_u32_e32 v106, vcc, s26, v122
	global_load_dwordx4 v[94:97], v[94:95], off nt
	s_nop 0
	global_load_dwordx4 v[102:105], v[102:103], off nt
	v_addc_co_u32_e32 v107, vcc, 0, v123, vcc
	v_add_co_u32_e32 v108, vcc, s27, v122
	s_nop 1
	v_addc_co_u32_e32 v109, vcc, 0, v123, vcc
	global_load_dwordx4 v[110:113], v[106:107], off nt
	global_load_dwordx4 v[118:121], v[108:109], off nt
	v_add_co_u32_e32 v106, vcc, 0x30000, v122
	s_nop 1
	v_addc_co_u32_e32 v107, vcc, 0, v123, vcc
	v_add_co_u32_e32 v114, vcc, 0x34000, v122
	s_nop 1
	v_addc_co_u32_e32 v115, vcc, 0, v123, vcc
	v_add_co_u32_e32 v124, vcc, 0x38000, v122
	global_load_dwordx4 v[106:109], v[106:107], off nt
	s_nop 0
	global_load_dwordx4 v[114:117], v[114:115], off nt
	v_addc_co_u32_e32 v125, vcc, 0, v123, vcc
	v_add_co_u32_e32 v126, vcc, 0x3c000, v122
	s_nop 1
	v_addc_co_u32_e32 v127, vcc, 0, v123, vcc
	global_load_dwordx4 v[122:125], v[124:125], off nt
	s_nop 0
	global_load_dwordx4 v[126:129], v[126:127], off nt
	s_branch .LBB0_220
.LBB0_227:
	v_readlane_b32 s0, v252, 14
	s_cmpk_gt_i32 s0, 0x1fff
	s_waitcnt vmcnt(62)
	v_lshlrev_b32_e32 v196, 2, v1
	s_cbranch_scc1 .LBB0_236
	s_waitcnt lgkmcnt(0)
	s_add_u32 s10, s82, 0x24000000
	v_readlane_b32 s33, v252, 14
	s_addc_u32 s11, s83, 0
	s_ashr_i32 s0, s33, 31
	s_lshr_b32 s0, s0, 24
	s_add_i32 s2, s33, s0
	s_ashr_i32 s0, s2, 8
	s_ashr_i32 s1, s0, 31
	s_lshl_b64 s[0:1], s[0:1], 24
	s_add_u32 s0, s14, s0
	s_addc_u32 s1, s15, s1
	s_and_b32 s2, s2, 0xffffff00
	s_sub_i32 s2, s33, s2
	s_lshr_b32 s3, s2, 3
	s_bfe_i32 s4, s3, 0x80000
	s_bfe_u32 s4, s4, 0x2000d
	s_add_i32 s4, s3, s4
	s_bfe_i32 s5, s4, 0x80000
	s_and_b32 s4, s4, 0xfc
	s_sub_i32 s3, s3, s4
	s_sext_i32_i8 s3, s3
	s_lshl_b32 s2, s2, 6
	s_lshl_b32 s3, s3, 9
	s_and_b32 s4, s2, 0x100
	s_sext_i32_i16 s5, s5
	s_or_b32 s3, s3, s4
	v_and_b32_e32 v137, 48, v0
	s_waitcnt vmcnt(31)
	v_or_b32_e32 v42, s3, v137
	s_lshl_b32 s3, s5, 6
	s_and_b32 s3, s3, 0xffffff00
	s_and_b32 s2, s2, 0xc0
	v_ashrrev_i32_e32 v43, 31, v42
	s_or_b32 s2, s3, s2
	v_lshlrev_b64 v[2:3], 13, v[42:43]
	s_ashr_i32 s3, s2, 31
	v_lshl_add_u64 v[2:3], s[0:1], 0, v[2:3]
	s_lshl_b64 s[2:3], s[2:3], 2
	v_mov_b32_e32 v197, 0
	v_lshl_add_u64 v[2:3], v[2:3], 0, s[2:3]
	v_lshlrev_b64 v[130:131], 2, v[196:197]
	v_lshl_add_u64 v[44:45], v[2:3], 0, v[130:131]
	s_movk_i32 s16, 0x2000
	v_add_co_u32_e32 v10, vcc, s16, v44
	s_movk_i32 s17, 0x4000
	s_nop 0
	v_addc_co_u32_e32 v11, vcc, 0, v45, vcc
	v_add_co_u32_e32 v14, vcc, s17, v44
	s_movk_i32 s18, 0x6000
	s_nop 0
	v_addc_co_u32_e32 v15, vcc, 0, v45, vcc
	v_add_co_u32_e32 v16, vcc, s18, v44
	s_mov_b32 s19, 0x8000
	s_nop 0
	v_addc_co_u32_e32 v17, vcc, 0, v45, vcc
	v_add_co_u32_e32 v26, vcc, s19, v44
	s_mov_b32 s20, 0xa000
	s_nop 0
	v_addc_co_u32_e32 v27, vcc, 0, v45, vcc
	v_add_co_u32_e32 v28, vcc, s20, v44
	s_mov_b32 s21, 0xc000
	s_nop 0
	v_addc_co_u32_e32 v29, vcc, 0, v45, vcc
	v_add_co_u32_e32 v30, vcc, s21, v44
	s_mov_b32 s22, 0xe000
	s_nop 0
	v_addc_co_u32_e32 v31, vcc, 0, v45, vcc
	v_add_co_u32_e32 v32, vcc, s22, v44
	s_mov_b32 s23, 0x10000
	s_nop 0
	v_addc_co_u32_e32 v33, vcc, 0, v45, vcc
	s_waitcnt vmcnt(30)
	v_add_co_u32_e32 v46, vcc, s23, v44
	s_mov_b32 s24, 0x12000
	s_nop 0
	v_addc_co_u32_e32 v47, vcc, 0, v45, vcc
	v_add_co_u32_e32 v48, vcc, s24, v44
	s_mov_b32 s25, 0x14000
	s_nop 0
	v_addc_co_u32_e32 v49, vcc, 0, v45, vcc
	global_load_dwordx4 v[2:5], v[44:45], off nt
	global_load_dwordx4 v[6:9], v[10:11], off nt
	s_nop 0
	global_load_dwordx4 v[10:13], v[14:15], off nt
	global_load_dwordx4 v[18:21], v[16:17], off nt
	s_nop 0
	global_load_dwordx4 v[14:17], v[26:27], off nt
	global_load_dwordx4 v[22:25], v[28:29], off nt
	s_nop 0
	global_load_dwordx4 v[26:29], v[30:31], off nt
	global_load_dwordx4 v[34:37], v[32:33], off nt
	s_nop 0
	global_load_dwordx4 v[30:33], v[46:47], off nt
	global_load_dwordx4 v[38:41], v[48:49], off nt
	v_add_co_u32_e32 v46, vcc, s25, v44
	s_mov_b32 s26, 0x16000
	s_nop 0
	v_addc_co_u32_e32 v47, vcc, 0, v45, vcc
	v_add_co_u32_e32 v48, vcc, s26, v44
	s_mov_b32 s27, 0x18000
	s_nop 0
	v_addc_co_u32_e32 v49, vcc, 0, v45, vcc
	global_load_dwordx4 v[54:57], v[46:47], off nt
	global_load_dwordx4 v[62:65], v[48:49], off nt
	v_add_co_u32_e32 v46, vcc, s27, v44
	s_mov_b32 s28, 0x1a000
	s_nop 0
	v_addc_co_u32_e32 v47, vcc, 0, v45, vcc
	v_add_co_u32_e32 v48, vcc, s28, v44
	v_or_b32_e32 v42, 64, v42
	s_nop 0
	v_addc_co_u32_e32 v49, vcc, 0, v45, vcc
	s_mov_b32 s29, 0x1c000
	v_ashrrev_i32_e32 v43, 31, v42
	global_load_dwordx4 v[50:53], v[46:47], off nt
	global_load_dwordx4 v[58:61], v[48:49], off nt
	v_add_co_u32_e32 v46, vcc, s29, v44
	v_lshlrev_b64 v[42:43], 13, v[42:43]
	s_nop 0
	v_addc_co_u32_e32 v47, vcc, 0, v45, vcc
	s_mov_b32 s30, 0x1e000
	v_lshl_add_u64 v[42:43], s[0:1], 0, v[42:43]
	v_add_co_u32_e32 v44, vcc, s30, v44
	v_lshl_add_u64 v[42:43], v[42:43], 0, s[2:3]
	s_nop 0
	v_addc_co_u32_e32 v45, vcc, 0, v45, vcc
	s_waitcnt vmcnt(31)
	v_lshl_add_u64 v[122:123], v[42:43], 0, v[130:131]
	s_waitcnt vmcnt(28)
	v_add_co_u32_e32 v66, vcc, s16, v122
	global_load_dwordx4 v[82:85], v[46:47], off nt
	global_load_dwordx4 v[86:89], v[44:45], off nt
	s_waitcnt vmcnt(29)
	v_addc_co_u32_e32 v67, vcc, 0, v123, vcc
	global_load_dwordx4 v[42:45], v[122:123], off nt
	global_load_dwordx4 v[46:49], v[66:67], off nt
	v_add_co_u32_e32 v66, vcc, s17, v122
	v_lshlrev_b32_e32 v132, 4, v1
	s_nop 0
	v_addc_co_u32_e32 v67, vcc, 0, v123, vcc
	s_waitcnt vmcnt(30)
	v_add_co_u32_e32 v68, vcc, s18, v122
	s_movk_i32 s0, 0x410
	s_waitcnt vmcnt(27)
	v_addc_co_u32_e32 v69, vcc, 0, v123, vcc
	v_add_co_u32_e32 v90, vcc, s19, v122
	global_load_dwordx4 v[70:73], v[66:67], off nt
	global_load_dwordx4 v[78:81], v[68:69], off nt
	v_addc_co_u32_e32 v91, vcc, 0, v123, vcc
	v_add_co_u32_e32 v92, vcc, s20, v122
	v_mov_b32_e32 v139, s6
	s_nop 0
	v_addc_co_u32_e32 v93, vcc, 0, v123, vcc
	v_add_co_u32_e32 v94, vcc, s21, v122
	global_load_dwordx4 v[66:69], v[90:91], off nt
	global_load_dwordx4 v[74:77], v[92:93], off nt
	v_addc_co_u32_e32 v95, vcc, 0, v123, vcc
	v_add_co_u32_e32 v96, vcc, s22, v122
	v_add_u32_e32 v134, s6, v137
	s_nop 0
	v_addc_co_u32_e32 v97, vcc, 0, v123, vcc
	v_add_co_u32_e32 v106, vcc, s23, v122
	global_load_dwordx4 v[90:93], v[94:95], off nt
	global_load_dwordx4 v[98:101], v[96:97], off nt
	v_addc_co_u32_e32 v107, vcc, 0, v123, vcc
	v_add_co_u32_e32 v108, vcc, s24, v122
	v_add_u32_e32 v135, s6, v132
	s_nop 0
	v_addc_co_u32_e32 v109, vcc, 0, v123, vcc
	global_load_dwordx4 v[94:97], v[106:107], off nt
	global_load_dwordx4 v[102:105], v[108:109], off nt
	v_add_co_u32_e32 v106, vcc, s25, v122
	v_mul_u32_u24_e32 v154, 0x410, v1
	s_nop 0
	v_addc_co_u32_e32 v107, vcc, 0, v123, vcc
	v_add_co_u32_e32 v108, vcc, s26, v122
	v_mad_u32_u24 v156, v1, s0, v139
	s_nop 0
	v_addc_co_u32_e32 v109, vcc, 0, v123, vcc
	global_load_dwordx4 v[110:113], v[106:107], off nt
	global_load_dwordx4 v[118:121], v[108:109], off nt
	v_add_co_u32_e32 v106, vcc, s27, v122
	v_mul_u32_u24_e32 v155, 0x104, v136
	s_nop 0
	v_addc_co_u32_e32 v107, vcc, 0, v123, vcc
	v_add_co_u32_e32 v114, vcc, s28, v122
	v_or_b32_e32 v138, 64, v137
	s_nop 0
	v_addc_co_u32_e32 v115, vcc, 0, v123, vcc
	v_add_co_u32_e32 v124, vcc, s29, v122
	global_load_dwordx4 v[106:109], v[106:107], off nt
	s_nop 0
	global_load_dwordx4 v[114:117], v[114:115], off nt
	v_addc_co_u32_e32 v125, vcc, 0, v123, vcc
	v_add_co_u32_e32 v126, vcc, s30, v122
	v_mov_b32_e32 v133, v197
	s_nop 0
	v_addc_co_u32_e32 v127, vcc, 0, v123, vcc
	global_load_dwordx4 v[122:125], v[124:125], off nt
	s_nop 0
	global_load_dwordx4 v[126:129], v[126:127], off nt
	v_or_b32_e32 v139, 4, v136
	v_or_b32_e32 v140, 8, v136
	v_or_b32_e32 v141, 12, v136
	v_or_b32_e32 v142, 16, v136
	v_or_b32_e32 v143, 20, v136
	v_or_b32_e32 v144, 24, v136
	v_or_b32_e32 v145, 28, v136
	v_or_b32_e32 v146, 32, v136
	v_or_b32_e32 v147, 36, v136
	v_or_b32_e32 v148, 40, v136
	v_or_b32_e32 v149, 44, v136
	v_or_b32_e32 v150, 48, v136
	v_or_b32_e32 v151, 52, v136
	v_or_b32_e32 v152, 56, v136
	v_or_b32_e32 v153, 60, v136
	s_lshl_b32 s34, s33, 6
	s_lshl_b32 s31, s85, 6
	v_add_u32_e32 v154, v134, v154
	v_add_u32_e32 v155, v135, v155
	v_add_u32_e32 v156, v156, v137
	s_branch .LBB0_230

.LBB0_230:
	s_waitcnt vmcnt(31)
	v_mul_f32_e32 v134, 0x42800000, v2
	s_waitcnt vmcnt(30)
	v_mul_f32_e32 v6, 0x42800000, v6
	v_mov_b32_e32 v2, 0
	v_cvt_pk_fp8_f32 v2, v134, v6
	v_mul_f32_e32 v3, 0x42800000, v3
	v_mul_f32_e32 v6, 0x42800000, v7
	v_mov_b32_e32 v7, 0
	v_cvt_pk_fp8_f32 v7, v3, v6
	s_waitcnt vmcnt(29)
	v_mul_f32_e32 v3, 0x42800000, v11
	s_waitcnt vmcnt(28)
	v_mul_f32_e32 v6, 0x42800000, v19
	v_mul_f32_e32 v10, 0x42800000, v10
	v_cvt_pk_fp8_f32 v7, v3, v6 op_sel:[0,0,1]
	v_mul_f32_e32 v3, 0x42800000, v4
	v_mul_f32_e32 v4, 0x42800000, v8
	v_mov_b32_e32 v6, 0
	v_cvt_pk_fp8_f32 v6, v3, v4
	v_mul_f32_e32 v18, 0x42800000, v18
	v_mul_f32_e32 v3, 0x42800000, v5
	v_mul_f32_e32 v4, 0x42800000, v9
	v_mov_b32_e32 v5, 0
	v_cvt_pk_fp8_f32 v2, v10, v18 op_sel:[0,0,1]
	v_mul_f32_e32 v8, 0x42800000, v12
	v_mul_f32_e32 v10, 0x42800000, v20
	v_cvt_pk_fp8_f32 v5, v3, v4
	v_cvt_pk_fp8_f32 v6, v8, v10 op_sel:[0,0,1]
	s_waitcnt vmcnt(27)
	v_mul_f32_e32 v9, 0x42800000, v15
	s_waitcnt vmcnt(26)
	v_mul_f32_e32 v10, 0x42800000, v23
	v_mov_b32_e32 v11, 0
	v_cvt_pk_fp8_f32 v11, v9, v10
	v_mul_f32_e32 v3, 0x42800000, v13
	v_mul_f32_e32 v4, 0x42800000, v21
	v_cvt_pk_fp8_f32 v5, v3, v4 op_sel:[0,0,1]
	v_mul_f32_e32 v4, 0x42800000, v14
	v_mul_f32_e32 v8, 0x42800000, v22
	v_mov_b32_e32 v3, 0
	v_cvt_pk_fp8_f32 v3, v4, v8
	s_waitcnt vmcnt(25)
	v_mul_f32_e32 v4, 0x42800000, v27
	s_waitcnt vmcnt(24)
	v_mul_f32_e32 v8, 0x42800000, v35
	v_cvt_pk_fp8_f32 v11, v4, v8 op_sel:[0,0,1]
	v_mul_f32_e32 v9, 0x42800000, v17
	v_mul_f32_e32 v10, 0x42800000, v25
	v_mul_f32_e32 v4, 0x42800000, v26
	ds_write2_b32 v154, v7, v11 offset0:65 offset1:66
	v_mov_b32_e32 v11, 0
	v_cvt_pk_fp8_f32 v11, v9, v10
	v_mul_f32_e32 v8, 0x42800000, v34
	v_cvt_pk_fp8_f32 v3, v4, v8 op_sel:[0,0,1]
	v_mul_f32_e32 v4, 0x42800000, v16
	v_mul_f32_e32 v8, 0x42800000, v24
	v_mov_b32_e32 v7, 0
	v_cvt_pk_fp8_f32 v7, v4, v8
	v_mul_f32_e32 v4, 0x42800000, v29
	v_mul_f32_e32 v8, 0x42800000, v37
	v_cvt_pk_fp8_f32 v11, v4, v8 op_sel:[0,0,1]
	v_mul_f32_e32 v4, 0x42800000, v28
	v_mul_f32_e32 v8, 0x42800000, v36
	v_cvt_pk_fp8_f32 v7, v4, v8 op_sel:[0,0,1]
	ds_write2_b32 v154, v5, v11 offset0:195 offset1:196
	s_waitcnt vmcnt(23)
	v_mul_f32_e32 v5, 0x42800000, v30
	s_waitcnt vmcnt(22)
	v_mul_f32_e32 v8, 0x42800000, v38
	v_mov_b32_e32 v4, 0
	v_cvt_pk_fp8_f32 v4, v5, v8
	v_mul_f32_e32 v5, 0x42800000, v31
	v_mul_f32_e32 v8, 0x42800000, v39
	v_mov_b32_e32 v11, 0
	v_cvt_pk_fp8_f32 v11, v5, v8
	s_mov_b32 s6, s33
	s_waitcnt vmcnt(21)
	v_mul_f32_e32 v9, 0x42800000, v54
	s_waitcnt vmcnt(20)
	v_mul_f32_e32 v10, 0x42800000, v62
	v_mul_f32_e32 v5, 0x42800000, v55
	v_mul_f32_e32 v8, 0x42800000, v63
	v_cvt_pk_fp8_f32 v4, v9, v10 op_sel:[0,0,1]
	v_cvt_pk_fp8_f32 v11, v5, v8 op_sel:[0,0,1]
	v_mul_f32_e32 v5, 0x42800000, v32
	v_mul_f32_e32 v9, 0x42800000, v40
	v_mov_b32_e32 v8, 0
	s_ashr_i32 s0, s6, 31
	v_cvt_pk_fp8_f32 v8, v5, v9
	v_mul_f32_e32 v5, 0x42800000, v33
	v_mul_f32_e32 v9, 0x42800000, v41
	v_mov_b32_e32 v13, 0
	s_lshr_b32 s0, s0, 24
	v_cvt_pk_fp8_f32 v13, v5, v9
	s_add_i32 s7, s6, s0
	s_ashr_i32 s2, s7, 8
	s_ashr_i32 s3, s2, 31
	s_add_i32 s33, s33, s85
	v_mul_f32_e32 v10, 0x42800000, v56
	v_mul_f32_e32 v12, 0x42800000, v64
	v_mul_f32_e32 v5, 0x42800000, v57
	v_mul_f32_e32 v9, 0x42800000, v65
	s_lshl_b64 s[0:1], s[2:3], 24
	v_cvt_pk_fp8_f32 v8, v10, v12 op_sel:[0,0,1]
	v_cvt_pk_fp8_f32 v13, v5, v9 op_sel:[0,0,1]
	s_waitcnt vmcnt(19)
	v_mul_f32_e32 v9, 0x42800000, v50
	s_waitcnt vmcnt(18)
	v_mul_f32_e32 v10, 0x42800000, v58
	v_mov_b32_e32 v5, 0
	s_add_u32 s4, s14, s0
	v_cvt_pk_fp8_f32 v5, v9, v10
	v_mul_f32_e32 v9, 0x42800000, v51
	v_mul_f32_e32 v10, 0x42800000, v59
	v_mov_b32_e32 v15, 0
	s_addc_u32 s5, s15, s1
	s_and_b32 s0, s7, 0x7ff00
	v_cvt_pk_fp8_f32 v15, v9, v10
	s_sub_i32 s0, s6, s0
	s_lshr_b32 s0, s0, 3
	s_bfe_i32 s1, s0, 0x80000
	s_waitcnt vmcnt(17)
	v_mul_f32_e32 v12, 0x42800000, v82
	s_waitcnt vmcnt(16)
	v_mul_f32_e32 v14, 0x42800000, v86
	v_mul_f32_e32 v9, 0x42800000, v83
	v_mul_f32_e32 v10, 0x42800000, v87
	s_bfe_u32 s1, s1, 0x2000d
	v_cvt_pk_fp8_f32 v5, v12, v14 op_sel:[0,0,1]
	v_cvt_pk_fp8_f32 v15, v9, v10 op_sel:[0,0,1]
	v_mul_f32_e32 v10, 0x42800000, v52
	v_mul_f32_e32 v12, 0x42800000, v60
	v_mov_b32_e32 v9, 0
	s_add_i32 s1, s0, s1
	v_cvt_pk_fp8_f32 v9, v10, v12
	v_mul_f32_e32 v10, 0x42800000, v53
	v_mul_f32_e32 v12, 0x42800000, v61
	v_mov_b32_e32 v17, 0
	s_bfe_i32 s6, s1, 0x80000
	s_and_b32 s1, s1, 0xfc
	v_cvt_pk_fp8_f32 v17, v10, v12
	s_sub_i32 s0, s0, s1
	s_lshl_b32 s1, s2, 14
	s_sext_i32_i8 s0, s0
	s_sub_i32 s1, s34, s1
	v_mul_f32_e32 v14, 0x42800000, v84
	v_mul_f32_e32 v16, 0x42800000, v88
	s_lshl_b32 s0, s0, 9
	s_and_b32 s7, s1, 0x100
	v_cvt_pk_fp8_f32 v9, v14, v16 op_sel:[0,0,1]
	v_mul_f32_e32 v10, 0x42800000, v85
	v_mul_f32_e32 v12, 0x42800000, v89
	s_sext_i32_i16 s6, s6
	s_or_b32 s35, s0, s7
	v_cvt_pk_fp8_f32 v17, v10, v12 op_sel:[0,0,1]
	v_or_b32_e32 v134, s35, v137
	s_lshl_b32 s0, s6, 6
	ds_write_b128 v154, v[2:5]
	ds_write2_b32 v154, v11, v15 offset0:67 offset1:68
	ds_write2_b64 v154, v[6:7], v[8:9] offset0:65 offset1:66
	ds_write2_b32 v154, v13, v17 offset0:197 offset1:198
	v_or_b32_e32 v2, 0x80, v134
	s_and_b32 s0, s0, 0xffffff00
	s_and_b32 s1, s1, 0xc0
	v_ashrrev_i32_e32 v3, 31, v2
	s_or_b32 s0, s0, s1
	v_lshlrev_b64 v[2:3], 13, v[2:3]
	s_ashr_i32 s1, s0, 31
	v_lshl_add_u64 v[2:3], s[4:5], 0, v[2:3]
	s_lshl_b64 s[6:7], s[0:1], 2
	v_lshl_add_u64 v[2:3], v[2:3], 0, s[6:7]
	v_lshl_add_u64 v[82:83], v[2:3], 0, v[130:131]
	v_add_co_u32_e32 v6, vcc, s16, v82
	s_waitcnt vmcnt(15)
	v_mul_f32_e32 v135, 0x42800000, v42
	v_addc_co_u32_e32 v7, vcc, 0, v83, vcc
	v_add_co_u32_e32 v10, vcc, s17, v82
	global_load_dwordx4 v[2:5], v[82:83], off nt
	s_nop 0
	global_load_dwordx4 v[6:9], v[6:7], off nt
	v_addc_co_u32_e32 v11, vcc, 0, v83, vcc
	v_add_co_u32_e32 v14, vcc, s18, v82
	s_waitcnt vmcnt(16)
	v_mul_f32_e32 v46, 0x42800000, v46
	v_addc_co_u32_e32 v15, vcc, 0, v83, vcc
	global_load_dwordx4 v[10:13], v[10:11], off nt
	s_nop 0
	global_load_dwordx4 v[18:21], v[14:15], off nt
	v_add_co_u32_e32 v14, vcc, s19, v82
	v_mov_b32_e32 v42, 0
	s_nop 0
	v_addc_co_u32_e32 v15, vcc, 0, v83, vcc
	v_add_co_u32_e32 v22, vcc, s20, v82
	v_cvt_pk_fp8_f32 v42, v135, v46
	s_nop 0
	v_addc_co_u32_e32 v23, vcc, 0, v83, vcc
	v_add_co_u32_e32 v26, vcc, s21, v82
	v_mul_f32_e32 v43, 0x42800000, v43
	v_mul_f32_e32 v46, 0x42800000, v47
	v_mov_b32_e32 v47, 0
	v_addc_co_u32_e32 v27, vcc, 0, v83, vcc
	v_cvt_pk_fp8_f32 v47, v43, v46
	v_add_co_u32_e32 v30, vcc, s22, v82
	global_load_dwordx4 v[14:17], v[14:15], off nt
	s_nop 0
	global_load_dwordx4 v[22:25], v[22:23], off nt
	v_addc_co_u32_e32 v31, vcc, 0, v83, vcc
	global_load_dwordx4 v[26:29], v[26:27], off nt
	s_nop 0
	global_load_dwordx4 v[34:37], v[30:31], off nt
	v_add_co_u32_e32 v30, vcc, s23, v82
	s_waitcnt vmcnt(21)
	v_mul_f32_e32 v43, 0x42800000, v71
	s_waitcnt vmcnt(20)
	v_mul_f32_e32 v46, 0x42800000, v79
	v_addc_co_u32_e32 v31, vcc, 0, v83, vcc
	v_cvt_pk_fp8_f32 v47, v43, v46 op_sel:[0,0,1]
	v_mul_f32_e32 v43, 0x42800000, v44
	v_mul_f32_e32 v44, 0x42800000, v48
	v_mov_b32_e32 v46, 0
	v_add_co_u32_e32 v38, vcc, s24, v82
	v_cvt_pk_fp8_f32 v46, v43, v44
	v_mul_f32_e32 v43, 0x42800000, v45
	v_mul_f32_e32 v44, 0x42800000, v49
	v_mov_b32_e32 v45, 0
	v_addc_co_u32_e32 v39, vcc, 0, v83, vcc
	v_cvt_pk_fp8_f32 v45, v43, v44
	v_add_co_u32_e32 v50, vcc, s25, v82
	v_mul_f32_e32 v43, 0x42800000, v73
	s_nop 0
	v_addc_co_u32_e32 v51, vcc, 0, v83, vcc
	v_add_co_u32_e32 v52, vcc, s26, v82
	v_mul_f32_e32 v44, 0x42800000, v81
	s_nop 0
	v_addc_co_u32_e32 v53, vcc, 0, v83, vcc
	v_cvt_pk_fp8_f32 v45, v43, v44 op_sel:[0,0,1]
	s_waitcnt vmcnt(19)
	v_mul_f32_e32 v44, 0x42800000, v66
	v_mul_f32_e32 v49, 0x42800000, v67
	s_waitcnt vmcnt(18)
	v_mul_f32_e32 v66, 0x42800000, v75
	v_mov_b32_e32 v67, 0
	global_load_dwordx4 v[30:33], v[30:31], off nt
	s_nop 0
	global_load_dwordx4 v[38:41], v[38:39], off nt
	s_nop 0
	global_load_dwordx4 v[54:57], v[50:51], off nt
	global_load_dwordx4 v[62:65], v[52:53], off nt
	v_add_co_u32_e32 v50, vcc, s27, v82
	v_mul_f32_e32 v70, 0x42800000, v70
	v_mul_f32_e32 v78, 0x42800000, v78
	v_cvt_pk_fp8_f32 v67, v49, v66
	v_addc_co_u32_e32 v51, vcc, 0, v83, vcc
	v_cvt_pk_fp8_f32 v42, v70, v78 op_sel:[0,0,1]
	v_mul_f32_e32 v48, 0x42800000, v72
	v_mul_f32_e32 v70, 0x42800000, v80
	v_add_co_u32_e32 v58, vcc, s28, v82
	v_cvt_pk_fp8_f32 v46, v48, v70 op_sel:[0,0,1]
	v_mul_f32_e32 v48, 0x42800000, v74
	v_mov_b32_e32 v43, 0
	v_addc_co_u32_e32 v59, vcc, 0, v83, vcc
	v_cvt_pk_fp8_f32 v43, v44, v48
	s_waitcnt vmcnt(21)
	v_mul_f32_e32 v44, 0x42800000, v91
	s_waitcnt vmcnt(20)
	v_mul_f32_e32 v48, 0x42800000, v99
	v_add_co_u32_e32 v84, vcc, s29, v82
	v_cvt_pk_fp8_f32 v67, v44, v48 op_sel:[0,0,1]
	s_nop 0
	v_addc_co_u32_e32 v85, vcc, 0, v83, vcc
	v_add_co_u32_e32 v86, vcc, s30, v82
	global_load_dwordx4 v[50:53], v[50:51], off nt
	s_nop 0
	global_load_dwordx4 v[58:61], v[58:59], off nt
	v_addc_co_u32_e32 v87, vcc, 0, v83, vcc
	global_load_dwordx4 v[82:85], v[84:85], off nt
	s_nop 0
	global_load_dwordx4 v[86:89], v[86:87], off nt
	ds_write2_b32 v156, v47, v67 offset0:81 offset1:82
	v_mul_f32_e32 v49, 0x42800000, v69
	v_mul_f32_e32 v66, 0x42800000, v77
	v_mov_b32_e32 v67, 0
	v_cvt_pk_fp8_f32 v67, v49, v66
	v_mul_f32_e32 v44, 0x42800000, v90
	v_mul_f32_e32 v48, 0x42800000, v98
	v_cvt_pk_fp8_f32 v43, v44, v48 op_sel:[0,0,1]
	v_mul_f32_e32 v44, 0x42800000, v68
	v_mul_f32_e32 v48, 0x42800000, v76
	v_mov_b32_e32 v47, 0
	v_cvt_pk_fp8_f32 v47, v44, v48
	v_mul_f32_e32 v44, 0x42800000, v93
	v_mul_f32_e32 v48, 0x42800000, v101
	v_cvt_pk_fp8_f32 v67, v44, v48 op_sel:[0,0,1]
	v_mul_f32_e32 v44, 0x42800000, v92
	v_mul_f32_e32 v48, 0x42800000, v100
	v_cvt_pk_fp8_f32 v47, v44, v48 op_sel:[0,0,1]
	ds_write2_b32 v156, v45, v67 offset0:211 offset1:212
	s_waitcnt vmcnt(23)
	v_mul_f32_e32 v45, 0x42800000, v94
	s_waitcnt vmcnt(22)
	v_mul_f32_e32 v48, 0x42800000, v102
	v_mov_b32_e32 v44, 0
	v_cvt_pk_fp8_f32 v44, v45, v48
	v_mul_f32_e32 v45, 0x42800000, v95
	v_mul_f32_e32 v48, 0x42800000, v103
	v_mov_b32_e32 v67, 0
	v_cvt_pk_fp8_f32 v67, v45, v48
	s_waitcnt vmcnt(21)
	v_mul_f32_e32 v49, 0x42800000, v110
	s_waitcnt vmcnt(20)
	v_mul_f32_e32 v66, 0x42800000, v118
	v_mul_f32_e32 v45, 0x42800000, v111
	v_mul_f32_e32 v48, 0x42800000, v119
	v_cvt_pk_fp8_f32 v44, v49, v66 op_sel:[0,0,1]
	v_cvt_pk_fp8_f32 v67, v45, v48 op_sel:[0,0,1]
	v_mul_f32_e32 v45, 0x42800000, v96
	v_mul_f32_e32 v49, 0x42800000, v104
	v_mov_b32_e32 v48, 0
	v_cvt_pk_fp8_f32 v48, v45, v49
	v_mul_f32_e32 v45, 0x42800000, v97
	v_mul_f32_e32 v49, 0x42800000, v105
	v_mov_b32_e32 v69, 0
	v_cvt_pk_fp8_f32 v69, v45, v49
	v_mul_f32_e32 v66, 0x42800000, v112
	v_mul_f32_e32 v68, 0x42800000, v120
	v_mul_f32_e32 v45, 0x42800000, v113
	v_mul_f32_e32 v49, 0x42800000, v121
	v_cvt_pk_fp8_f32 v48, v66, v68 op_sel:[0,0,1]
	v_cvt_pk_fp8_f32 v69, v45, v49 op_sel:[0,0,1]
	s_waitcnt vmcnt(19)
	v_mul_f32_e32 v49, 0x42800000, v106
	s_waitcnt vmcnt(18)
	v_mul_f32_e32 v66, 0x42800000, v114
	v_mov_b32_e32 v45, 0
	v_cvt_pk_fp8_f32 v45, v49, v66
	v_mul_f32_e32 v49, 0x42800000, v107
	v_mul_f32_e32 v66, 0x42800000, v115
	v_mov_b32_e32 v71, 0
	v_cvt_pk_fp8_f32 v71, v49, v66
	s_waitcnt vmcnt(17)
	v_mul_f32_e32 v68, 0x42800000, v122
	s_waitcnt vmcnt(16)
	v_mul_f32_e32 v70, 0x42800000, v126
	v_mul_f32_e32 v49, 0x42800000, v123
	v_mul_f32_e32 v66, 0x42800000, v127
	v_cvt_pk_fp8_f32 v45, v68, v70 op_sel:[0,0,1]
	v_cvt_pk_fp8_f32 v71, v49, v66 op_sel:[0,0,1]
	v_mul_f32_e32 v66, 0x42800000, v108
	v_mul_f32_e32 v68, 0x42800000, v116
	v_mov_b32_e32 v49, 0
	v_cvt_pk_fp8_f32 v49, v66, v68
	v_mul_f32_e32 v66, 0x42800000, v109
	v_mul_f32_e32 v68, 0x42800000, v117
	v_mov_b32_e32 v73, 0
	v_cvt_pk_fp8_f32 v73, v66, v68
	v_mul_f32_e32 v70, 0x42800000, v124
	v_mul_f32_e32 v72, 0x42800000, v128
	v_cvt_pk_fp8_f32 v49, v70, v72 op_sel:[0,0,1]
	v_mul_f32_e32 v66, 0x42800000, v125
	v_mul_f32_e32 v68, 0x42800000, v129
	v_cvt_pk_fp8_f32 v73, v66, v68 op_sel:[0,0,1]
	ds_write_b128 v156, v[42:45] offset:64
	ds_write2_b32 v156, v67, v71 offset0:83 offset1:84
	ds_write2_b64 v156, v[46:47], v[48:49] offset0:73 offset1:74
	ds_write2_b32 v156, v69, v73 offset0:213 offset1:214
	v_or_b32_e32 v42, 0xc0, v134
	v_ashrrev_i32_e32 v43, 31, v42
	v_lshlrev_b64 v[42:43], 13, v[42:43]
	v_lshl_add_u64 v[42:43], s[4:5], 0, v[42:43]
	v_lshl_add_u64 v[42:43], v[42:43], 0, s[6:7]
	v_lshl_add_u64 v[122:123], v[42:43], 0, v[130:131]
	v_add_co_u32_e32 v46, vcc, s16, v122
	s_waitcnt vmcnt(15)
	v_mul_f32_e32 v134, 0x42800000, v2
	v_addc_co_u32_e32 v47, vcc, 0, v123, vcc
	v_add_co_u32_e32 v66, vcc, s17, v122
	global_load_dwordx4 v[42:45], v[122:123], off nt
	s_nop 0
	global_load_dwordx4 v[46:49], v[46:47], off nt
	v_addc_co_u32_e32 v67, vcc, 0, v123, vcc
	v_add_co_u32_e32 v68, vcc, s18, v122
	s_waitcnt vmcnt(16)
	v_mul_f32_e32 v135, 0x42800000, v6
	v_addc_co_u32_e32 v69, vcc, 0, v123, vcc
	global_load_dwordx4 v[70:73], v[66:67], off nt
	global_load_dwordx4 v[78:81], v[68:69], off nt
	v_add_co_u32_e32 v66, vcc, s19, v122
	v_mov_b32_e32 v158, 0
	s_nop 0
	v_addc_co_u32_e32 v67, vcc, 0, v123, vcc
	v_add_co_u32_e32 v74, vcc, s20, v122
	v_cvt_pk_fp8_f32 v158, v134, v135
	s_nop 0
	v_addc_co_u32_e32 v75, vcc, 0, v123, vcc
	v_add_co_u32_e32 v90, vcc, s21, v122
	global_load_dwordx4 v[66:69], v[66:67], off nt
	s_nop 0
	global_load_dwordx4 v[74:77], v[74:75], off nt
	v_addc_co_u32_e32 v91, vcc, 0, v123, vcc
	v_add_co_u32_e32 v94, vcc, s22, v122
	v_mul_f32_e32 v134, 0x42800000, v3
	s_nop 0
	v_addc_co_u32_e32 v95, vcc, 0, v123, vcc
	global_load_dwordx4 v[90:93], v[90:91], off nt
	s_nop 0
	global_load_dwordx4 v[98:101], v[94:95], off nt
	v_add_co_u32_e32 v94, vcc, s23, v122
	v_mul_f32_e32 v135, 0x42800000, v7
	s_nop 0
	v_addc_co_u32_e32 v95, vcc, 0, v123, vcc
	v_add_co_u32_e32 v102, vcc, s24, v122
	v_mov_b32_e32 v160, 0
	s_nop 0
	v_addc_co_u32_e32 v103, vcc, 0, v123, vcc
	v_add_co_u32_e32 v106, vcc, s25, v122
	global_load_dwordx4 v[94:97], v[94:95], off nt
	s_nop 0
	global_load_dwordx4 v[102:105], v[102:103], off nt
	v_addc_co_u32_e32 v107, vcc, 0, v123, vcc
	v_add_co_u32_e32 v108, vcc, s26, v122
	v_cvt_pk_fp8_f32 v160, v134, v135
	s_nop 0
	v_addc_co_u32_e32 v109, vcc, 0, v123, vcc
	global_load_dwordx4 v[110:113], v[106:107], off nt
	global_load_dwordx4 v[118:121], v[108:109], off nt
	v_add_co_u32_e32 v106, vcc, s27, v122
	s_waitcnt vmcnt(25)
	v_mul_f32_e32 v157, 0x42800000, v10
	v_addc_co_u32_e32 v107, vcc, 0, v123, vcc
	v_add_co_u32_e32 v114, vcc, s28, v122
	s_waitcnt vmcnt(24)
	v_mul_f32_e32 v159, 0x42800000, v18
	v_addc_co_u32_e32 v115, vcc, 0, v123, vcc
	v_add_co_u32_e32 v124, vcc, s29, v122
	global_load_dwordx4 v[106:109], v[106:107], off nt
	s_nop 0
	global_load_dwordx4 v[114:117], v[114:115], off nt
	v_addc_co_u32_e32 v125, vcc, 0, v123, vcc
	v_add_co_u32_e32 v126, vcc, s30, v122
	v_mul_f32_e32 v134, 0x42800000, v11
	s_nop 0
	v_addc_co_u32_e32 v127, vcc, 0, v123, vcc
	global_load_dwordx4 v[122:125], v[124:125], off nt
	s_nop 0
	global_load_dwordx4 v[126:129], v[126:127], off nt
	v_mul_f32_e32 v135, 0x42800000, v19
	v_cvt_pk_fp8_f32 v158, v157, v159 op_sel:[0,0,1]
	v_cvt_pk_fp8_f32 v160, v134, v135 op_sel:[0,0,1]
	v_mul_f32_e32 v135, 0x42800000, v4
	v_mul_f32_e32 v157, 0x42800000, v8
	v_mov_b32_e32 v134, 0
	v_cvt_pk_fp8_f32 v134, v135, v157
	v_mul_f32_e32 v135, 0x42800000, v5
	v_mul_f32_e32 v157, 0x42800000, v9
	v_mov_b32_e32 v162, 0
	v_mul_f32_e32 v159, 0x42800000, v12
	v_mul_f32_e32 v161, 0x42800000, v20
	v_cvt_pk_fp8_f32 v162, v135, v157
	v_cvt_pk_fp8_f32 v134, v159, v161 op_sel:[0,0,1]
	s_waitcnt vmcnt(27)
	v_mul_f32_e32 v161, 0x42800000, v15
	s_waitcnt vmcnt(26)
	v_mul_f32_e32 v163, 0x42800000, v23
	v_mov_b32_e32 v164, 0
	v_cvt_pk_fp8_f32 v164, v161, v163
	v_mul_f32_e32 v135, 0x42800000, v13
	v_mul_f32_e32 v157, 0x42800000, v21
	v_cvt_pk_fp8_f32 v162, v135, v157 op_sel:[0,0,1]
	v_mul_f32_e32 v135, 0x42800000, v14
	v_mul_f32_e32 v157, 0x42800000, v22
	v_mov_b32_e32 v159, 0
	v_cvt_pk_fp8_f32 v159, v135, v157
	s_waitcnt vmcnt(25)
	v_mul_f32_e32 v135, 0x42800000, v27
	s_waitcnt vmcnt(24)
	v_mul_f32_e32 v157, 0x42800000, v35
	v_cvt_pk_fp8_f32 v164, v135, v157 op_sel:[0,0,1]
	v_mul_f32_e32 v161, 0x42800000, v17
	v_mul_f32_e32 v163, 0x42800000, v25
	v_mul_f32_e32 v135, 0x42800000, v26
	ds_write2_b32 v156, v160, v164 offset0:97 offset1:98
	v_mov_b32_e32 v164, 0
	v_cvt_pk_fp8_f32 v164, v161, v163
	v_mul_f32_e32 v157, 0x42800000, v34
	v_cvt_pk_fp8_f32 v159, v135, v157 op_sel:[0,0,1]
	v_mul_f32_e32 v157, 0x42800000, v16
	v_mul_f32_e32 v160, 0x42800000, v24
	v_mov_b32_e32 v135, 0
	v_cvt_pk_fp8_f32 v135, v157, v160
	v_mul_f32_e32 v157, 0x42800000, v29
	v_mul_f32_e32 v160, 0x42800000, v37
	v_cvt_pk_fp8_f32 v164, v157, v160 op_sel:[0,0,1]
	v_mul_f32_e32 v157, 0x42800000, v28
	v_mul_f32_e32 v160, 0x42800000, v36
	v_cvt_pk_fp8_f32 v135, v157, v160 op_sel:[0,0,1]
	s_waitcnt vmcnt(23)
	v_mul_f32_e32 v157, 0x42800000, v30
	s_waitcnt vmcnt(22)
	v_mul_f32_e32 v161, 0x42800000, v38
	v_mov_b32_e32 v160, 0
	ds_write2_b32 v156, v162, v164 offset0:227 offset1:228
	v_cvt_pk_fp8_f32 v160, v157, v161
	v_mul_f32_e32 v157, 0x42800000, v31
	v_mul_f32_e32 v161, 0x42800000, v39
	v_mov_b32_e32 v164, 0
	v_cvt_pk_fp8_f32 v164, v157, v161
	s_waitcnt vmcnt(21)
	v_mul_f32_e32 v162, 0x42800000, v54
	s_waitcnt vmcnt(20)
	v_mul_f32_e32 v163, 0x42800000, v62
	v_mul_f32_e32 v157, 0x42800000, v55
	v_mul_f32_e32 v161, 0x42800000, v63
	v_cvt_pk_fp8_f32 v160, v162, v163 op_sel:[0,0,1]
	v_cvt_pk_fp8_f32 v164, v157, v161 op_sel:[0,0,1]
	v_mul_f32_e32 v157, 0x42800000, v32
	v_mul_f32_e32 v161, 0x42800000, v40
	v_mov_b32_e32 v162, 0
	v_cvt_pk_fp8_f32 v162, v157, v161
	v_mul_f32_e32 v157, 0x42800000, v33
	v_mul_f32_e32 v161, 0x42800000, v41
	v_mov_b32_e32 v166, 0
	v_cvt_pk_fp8_f32 v166, v157, v161
	v_mul_f32_e32 v163, 0x42800000, v56
	v_mul_f32_e32 v165, 0x42800000, v64
	v_mul_f32_e32 v157, 0x42800000, v57
	v_mul_f32_e32 v161, 0x42800000, v65
	v_cvt_pk_fp8_f32 v162, v163, v165 op_sel:[0,0,1]
	v_cvt_pk_fp8_f32 v166, v157, v161 op_sel:[0,0,1]
	s_waitcnt vmcnt(19)
	v_mul_f32_e32 v157, 0x42800000, v50
	s_waitcnt vmcnt(18)
	v_mul_f32_e32 v163, 0x42800000, v58
	v_mov_b32_e32 v161, 0
	v_cvt_pk_fp8_f32 v161, v157, v163
	v_mul_f32_e32 v157, 0x42800000, v51
	v_mul_f32_e32 v163, 0x42800000, v59
	v_mov_b32_e32 v168, 0
	v_cvt_pk_fp8_f32 v168, v157, v163
	s_waitcnt vmcnt(17)
	v_mul_f32_e32 v165, 0x42800000, v82
	s_waitcnt vmcnt(16)
	v_mul_f32_e32 v167, 0x42800000, v86
	v_mul_f32_e32 v157, 0x42800000, v83
	v_mul_f32_e32 v163, 0x42800000, v87
	v_cvt_pk_fp8_f32 v161, v165, v167 op_sel:[0,0,1]
	v_cvt_pk_fp8_f32 v168, v157, v163 op_sel:[0,0,1]
	v_mul_f32_e32 v157, 0x42800000, v52
	v_mul_f32_e32 v165, 0x42800000, v60
	v_mov_b32_e32 v163, 0
	v_cvt_pk_fp8_f32 v163, v157, v165
	v_mul_f32_e32 v157, 0x42800000, v53
	v_mul_f32_e32 v165, 0x42800000, v61
	v_mov_b32_e32 v170, 0
	v_cvt_pk_fp8_f32 v170, v157, v165
	v_mul_f32_e32 v167, 0x42800000, v84
	v_mul_f32_e32 v169, 0x42800000, v88
	s_cmpk_gt_i32 s33, 0x1fff
	v_cvt_pk_fp8_f32 v163, v167, v169 op_sel:[0,0,1]
	v_mul_f32_e32 v157, 0x42800000, v85
	v_mul_f32_e32 v165, 0x42800000, v89
	s_cselect_b64 s[4:5], -1, 0
	v_cvt_pk_fp8_f32 v170, v157, v165 op_sel:[0,0,1]
	s_and_b64 vcc, exec, s[4:5]
	ds_write_b128 v156, v[158:161] offset:128
	ds_write2_b32 v156, v164, v168 offset0:99 offset1:100
	ds_write2_b64 v156, v[134:135], v[162:163] offset0:81 offset1:82
	ds_write2_b32 v156, v166, v170 offset0:229 offset1:230
	s_cbranch_vccnz .LBB0_232
	s_ashr_i32 s1, s33, 31
	s_lshr_b32 s1, s1, 24
	s_add_i32 s1, s33, s1
	s_ashr_i32 s6, s1, 8
	s_ashr_i32 s7, s6, 31
	s_lshl_b64 s[6:7], s[6:7], 24
	s_add_u32 s6, s14, s6
	s_addc_u32 s7, s15, s7
	s_and_b32 s1, s1, 0xffffff00
	s_sub_i32 s1, s33, s1
	s_lshr_b32 s8, s1, 3
	s_bfe_i32 s9, s8, 0x80000
	s_bfe_u32 s9, s9, 0x2000d
	s_add_i32 s9, s8, s9
	s_bfe_i32 s36, s9, 0x80000
	s_and_b32 s9, s9, 0xfc
	s_sub_i32 s8, s8, s9
	s_sext_i32_i8 s8, s8
	s_lshl_b32 s1, s1, 6
	s_lshl_b32 s8, s8, 9
	s_and_b32 s9, s1, 0x100
	s_or_b32 s8, s8, s9
	v_or_b32_e32 v2, s8, v137
	v_ashrrev_i32_e32 v3, 31, v2
	s_sext_i32_i16 s36, s36
	v_lshlrev_b64 v[2:3], 13, v[2:3]
	v_lshl_add_u64 v[2:3], s[6:7], 0, v[2:3]
	s_lshl_b32 s6, s36, 6
	s_and_b32 s6, s6, 0xffffff00
	s_and_b32 s1, s1, 0xc0
	s_or_b32 s6, s6, s1
	s_ashr_i32 s7, s6, 31
	v_lshl_add_u64 v[2:3], s[6:7], 2, v[2:3]
	v_lshl_add_u64 v[82:83], v[196:197], 2, v[2:3]
	v_add_co_u32_e32 v6, vcc, s16, v82
	s_nop 1
	v_addc_co_u32_e32 v7, vcc, 0, v83, vcc
	v_add_co_u32_e32 v10, vcc, s17, v82
	global_load_dwordx4 v[2:5], v[82:83], off nt
	s_nop 0
	global_load_dwordx4 v[6:9], v[6:7], off nt
	v_addc_co_u32_e32 v11, vcc, 0, v83, vcc
	v_add_co_u32_e32 v14, vcc, s18, v82
	s_nop 1
	v_addc_co_u32_e32 v15, vcc, 0, v83, vcc
	global_load_dwordx4 v[10:13], v[10:11], off nt
	s_nop 0
	global_load_dwordx4 v[18:21], v[14:15], off nt
	v_add_co_u32_e32 v14, vcc, s19, v82
	s_nop 1
	v_addc_co_u32_e32 v15, vcc, 0, v83, vcc
	v_add_co_u32_e32 v22, vcc, s20, v82
	s_nop 1
	v_addc_co_u32_e32 v23, vcc, 0, v83, vcc
	v_add_co_u32_e32 v26, vcc, s21, v82
	global_load_dwordx4 v[14:17], v[14:15], off nt
	s_nop 0
	global_load_dwordx4 v[22:25], v[22:23], off nt
	v_addc_co_u32_e32 v27, vcc, 0, v83, vcc
	v_add_co_u32_e32 v30, vcc, s22, v82
	s_nop 1
	v_addc_co_u32_e32 v31, vcc, 0, v83, vcc
	global_load_dwordx4 v[26:29], v[26:27], off nt
	s_nop 0
	global_load_dwordx4 v[34:37], v[30:31], off nt
	v_add_co_u32_e32 v30, vcc, s23, v82
	s_nop 1
	v_addc_co_u32_e32 v31, vcc, 0, v83, vcc
	v_add_co_u32_e32 v38, vcc, s24, v82
	s_nop 1
	v_addc_co_u32_e32 v39, vcc, 0, v83, vcc
	v_add_co_u32_e32 v50, vcc, s25, v82
	global_load_dwordx4 v[30:33], v[30:31], off nt
	s_nop 0
	global_load_dwordx4 v[38:41], v[38:39], off nt
	v_addc_co_u32_e32 v51, vcc, 0, v83, vcc
	v_add_co_u32_e32 v52, vcc, s26, v82
	s_nop 1
	v_addc_co_u32_e32 v53, vcc, 0, v83, vcc
	global_load_dwordx4 v[54:57], v[50:51], off nt
	global_load_dwordx4 v[62:65], v[52:53], off nt
	v_add_co_u32_e32 v50, vcc, 0x18000, v82
	s_nop 1
	v_addc_co_u32_e32 v51, vcc, 0, v83, vcc
	v_add_co_u32_e32 v58, vcc, 0x1a000, v82
	s_nop 1
	v_addc_co_u32_e32 v59, vcc, 0, v83, vcc
	v_add_co_u32_e32 v84, vcc, 0x1c000, v82
	global_load_dwordx4 v[50:53], v[50:51], off nt
	s_nop 0
	global_load_dwordx4 v[58:61], v[58:59], off nt
	v_addc_co_u32_e32 v85, vcc, 0, v83, vcc
	v_add_co_u32_e32 v86, vcc, 0x1e000, v82
	s_nop 1
	v_addc_co_u32_e32 v87, vcc, 0, v83, vcc
	global_load_dwordx4 v[82:85], v[84:85], off nt
	s_nop 0
	global_load_dwordx4 v[86:89], v[86:87], off nt

.LBB0_234:
	s_andn2_b64 vcc, exec, s[4:5]
	s_lshl_b64 s[2:3], s[2:3], 22
	s_cbranch_vccnz .LBB0_229
	s_ashr_i32 s1, s33, 31
	s_lshr_b32 s1, s1, 24
	s_add_i32 s1, s33, s1
	s_ashr_i32 s4, s1, 8
	s_ashr_i32 s5, s4, 31
	s_lshl_b64 s[6:7], s[4:5], 24
	s_add_u32 s6, s14, s6
	s_addc_u32 s7, s15, s7
	s_and_b32 s1, s1, 0x7ff00
	s_sub_i32 s1, s33, s1
	s_lshr_b32 s1, s1, 3
	s_bfe_i32 s5, s1, 0x80000
	s_bfe_u32 s5, s5, 0x2000d
	s_add_i32 s5, s1, s5
	s_bfe_i32 s36, s5, 0x80000
	s_and_b32 s5, s5, 0xfc
	s_sub_i32 s1, s1, s5
	s_sext_i32_i8 s1, s1
	s_lshl_b32 s5, s1, 9
	s_add_i32 s1, s31, s34
	s_lshl_b32 s4, s4, 14
	s_sub_i32 s4, s1, s4
	s_and_b32 s34, s4, 0x100
	s_sext_i32_i16 s36, s36
	s_or_b32 s5, s5, s34
	v_or_b32_e32 v42, s5, v138
	s_lshl_b32 s5, s36, 6
	v_ashrrev_i32_e32 v43, 31, v42
	s_and_b32 s5, s5, 0xffffff00
	s_and_b32 s4, s4, 0xc0
	v_lshlrev_b64 v[42:43], 13, v[42:43]
	s_or_b32 s4, s5, s4
	v_lshl_add_u64 v[42:43], s[6:7], 0, v[42:43]
	s_ashr_i32 s5, s4, 31
	v_lshl_add_u64 v[42:43], s[4:5], 2, v[42:43]
	v_lshl_add_u64 v[122:123], v[196:197], 2, v[42:43]
	v_add_co_u32_e32 v46, vcc, s16, v122
	s_nop 1
	v_addc_co_u32_e32 v47, vcc, 0, v123, vcc
	v_add_co_u32_e32 v66, vcc, s17, v122
	global_load_dwordx4 v[42:45], v[122:123], off nt
	s_nop 0
	global_load_dwordx4 v[46:49], v[46:47], off nt
	v_addc_co_u32_e32 v67, vcc, 0, v123, vcc
	v_add_co_u32_e32 v68, vcc, s18, v122
	s_nop 1
	v_addc_co_u32_e32 v69, vcc, 0, v123, vcc
	global_load_dwordx4 v[70:73], v[66:67], off nt
	global_load_dwordx4 v[78:81], v[68:69], off nt
	v_add_co_u32_e32 v66, vcc, s19, v122
	s_nop 1
	v_addc_co_u32_e32 v67, vcc, 0, v123, vcc
	v_add_co_u32_e32 v74, vcc, s20, v122
	s_nop 1
	v_addc_co_u32_e32 v75, vcc, 0, v123, vcc
	v_add_co_u32_e32 v90, vcc, s21, v122
	global_load_dwordx4 v[66:69], v[66:67], off nt
	s_nop 0
	global_load_dwordx4 v[74:77], v[74:75], off nt
	v_addc_co_u32_e32 v91, vcc, 0, v123, vcc
	v_add_co_u32_e32 v94, vcc, s22, v122
	s_nop 1
	v_addc_co_u32_e32 v95, vcc, 0, v123, vcc
	global_load_dwordx4 v[90:93], v[90:91], off nt
	s_nop 0
	global_load_dwordx4 v[98:101], v[94:95], off nt
	v_add_co_u32_e32 v94, vcc, s23, v122
	s_nop 1
	v_addc_co_u32_e32 v95, vcc, 0, v123, vcc
	v_add_co_u32_e32 v102, vcc, s24, v122
	s_nop 1
	v_addc_co_u32_e32 v103, vcc, 0, v123, vcc
	v_add_co_u32_e32 v106, vcc, s25, v122
	global_load_dwordx4 v[94:97], v[94:95], off nt
	s_nop 0
	global_load_dwordx4 v[102:105], v[102:103], off nt
	v_addc_co_u32_e32 v107, vcc, 0, v123, vcc
	v_add_co_u32_e32 v108, vcc, s26, v122
	s_nop 1
	v_addc_co_u32_e32 v109, vcc, 0, v123, vcc
	global_load_dwordx4 v[110:113], v[106:107], off nt
	global_load_dwordx4 v[118:121], v[108:109], off nt
	v_add_co_u32_e32 v106, vcc, 0x18000, v122
	s_nop 1
	v_addc_co_u32_e32 v107, vcc, 0, v123, vcc
	v_add_co_u32_e32 v114, vcc, 0x1a000, v122
	s_nop 1
	v_addc_co_u32_e32 v115, vcc, 0, v123, vcc
	v_add_co_u32_e32 v124, vcc, 0x1c000, v122
	global_load_dwordx4 v[106:109], v[106:107], off nt
	s_nop 0
	global_load_dwordx4 v[114:117], v[114:115], off nt
	v_addc_co_u32_e32 v125, vcc, 0, v123, vcc
	v_add_co_u32_e32 v126, vcc, 0x1e000, v122
	s_nop 1
	v_addc_co_u32_e32 v127, vcc, 0, v123, vcc
	global_load_dwordx4 v[122:125], v[124:125], off nt
	s_nop 0
	global_load_dwordx4 v[126:129], v[126:127], off nt
	s_branch .LBB0_229
